# gemm2 mid hook: all 32 gate loads touched at hook start (L2 warm) on top of v24
# baseline (speedup 1.0000x reference)
.LBB0_599:
	s_andn2_b64 vcc, exec, s[50:51]
	s_cbranch_vccnz .LBB0_601
	v_mov_b32_e32 v5, v202
	s_nop 15
	s_nop 15
	s_nop 15
	s_nop 15
	global_load_dwordx4 v[6:9], v[168:169], off offset:16
	global_load_dwordx4 v[14:17], v[168:169], off
	global_load_dwordx4 v[10:13], v[164:165], off offset:16
	global_load_dwordx4 v[18:21], v[164:165], off
	v_mad_i64_i32 v[178:179], s[50:51], v5, s94, v[166:167]
	v_mov_b64_e32 v[156:157], v[178:179]
	s_mov_b64 s[100:101], 0x2000
	v_lshl_add_u64 v[182:183], v[156:157], 0, s[100:101]
	global_load_dwordx2 v[180:181], v[182:183], off offset:1024
	global_load_dwordx2 v[180:181], v[182:183], off offset:3072
	s_mov_b64 s[100:101], 0x36000
	v_lshl_add_u64 v[182:183], v[156:157], 0, s[100:101]
	global_load_dwordx2 v[180:181], v[182:183], off offset:1024
	global_load_dwordx2 v[180:181], v[182:183], off offset:3072
	s_mov_b64 s[100:101], 0x6a000
	v_lshl_add_u64 v[182:183], v[156:157], 0, s[100:101]
	global_load_dwordx2 v[180:181], v[182:183], off offset:1024
	global_load_dwordx2 v[180:181], v[182:183], off offset:3072
	s_mov_b64 s[100:101], 0x9e000
	v_lshl_add_u64 v[182:183], v[156:157], 0, s[100:101]
	global_load_dwordx2 v[180:181], v[182:183], off offset:1024
	global_load_dwordx2 v[180:181], v[182:183], off offset:3072
	s_mov_b64 s[100:101], 0x2080
	v_lshl_add_u64 v[182:183], v[156:157], 0, s[100:101]
	global_load_dwordx2 v[180:181], v[182:183], off offset:1024
	global_load_dwordx2 v[180:181], v[182:183], off offset:3072
	s_mov_b64 s[100:101], 0x36080
	v_lshl_add_u64 v[182:183], v[156:157], 0, s[100:101]
	global_load_dwordx2 v[180:181], v[182:183], off offset:1024
	global_load_dwordx2 v[180:181], v[182:183], off offset:3072
	s_mov_b64 s[100:101], 0x6a080
	v_lshl_add_u64 v[182:183], v[156:157], 0, s[100:101]
	global_load_dwordx2 v[180:181], v[182:183], off offset:1024
	global_load_dwordx2 v[180:181], v[182:183], off offset:3072
	s_mov_b64 s[100:101], 0x9e080
	v_lshl_add_u64 v[182:183], v[156:157], 0, s[100:101]
	global_load_dwordx2 v[180:181], v[182:183], off offset:1024
	global_load_dwordx2 v[180:181], v[182:183], off offset:3072
	s_mov_b64 s[100:101], 0x1a2000
	v_lshl_add_u64 v[182:183], v[156:157], 0, s[100:101]
	global_load_dwordx2 v[180:181], v[182:183], off offset:1024
	global_load_dwordx2 v[180:181], v[182:183], off offset:3072
	s_mov_b64 s[100:101], 0x1d6000
	v_lshl_add_u64 v[182:183], v[156:157], 0, s[100:101]
	global_load_dwordx2 v[180:181], v[182:183], off offset:1024
	global_load_dwordx2 v[180:181], v[182:183], off offset:3072
	s_mov_b64 s[100:101], 0x20a000
	v_lshl_add_u64 v[182:183], v[156:157], 0, s[100:101]
	global_load_dwordx2 v[180:181], v[182:183], off offset:1024
	global_load_dwordx2 v[180:181], v[182:183], off offset:3072
	s_mov_b64 s[100:101], 0x23e000
	v_lshl_add_u64 v[182:183], v[156:157], 0, s[100:101]
	global_load_dwordx2 v[180:181], v[182:183], off offset:1024
	global_load_dwordx2 v[180:181], v[182:183], off offset:3072
	s_mov_b64 s[100:101], 0x1a2080
	v_lshl_add_u64 v[182:183], v[156:157], 0, s[100:101]
	global_load_dwordx2 v[180:181], v[182:183], off offset:1024
	global_load_dwordx2 v[180:181], v[182:183], off offset:3072
	s_mov_b64 s[100:101], 0x1d6080
	v_lshl_add_u64 v[182:183], v[156:157], 0, s[100:101]
	global_load_dwordx2 v[180:181], v[182:183], off offset:1024
	global_load_dwordx2 v[180:181], v[182:183], off offset:3072
	s_mov_b64 s[100:101], 0x20a080
	v_lshl_add_u64 v[182:183], v[156:157], 0, s[100:101]
	global_load_dwordx2 v[180:181], v[182:183], off offset:1024
	global_load_dwordx2 v[180:181], v[182:183], off offset:3072
	s_mov_b64 s[100:101], 0x23e080
	v_lshl_add_u64 v[182:183], v[156:157], 0, s[100:101]
	global_load_dwordx2 v[180:181], v[182:183], off offset:1024
	global_load_dwordx2 v[180:181], v[182:183], off offset:3072
	s_mov_b64 s[50:51], 0x1a0000
	v_add_co_u32_e32 v158, vcc, s31, v156
	s_nop 1
	v_addc_co_u32_e32 v159, vcc, 0, v157, vcc
	flat_load_dwordx2 v[160:161], v[158:159] offset:1024
	s_nop 0
	flat_load_dwordx2 v[158:159], v[158:159] offset:3072
	v_add_co_u32_e32 v162, vcc, s20, v156
	s_waitcnt vmcnt(0) lgkmcnt(0)
	v_cvt_pk_f32_fp8_e32 v[196:197], v161
	v_addc_co_u32_e32 v163, vcc, 0, v157, vcc
	flat_load_dwordx2 v[190:191], v[162:163] offset:1024
	flat_load_dwordx2 v[188:189], v[162:163] offset:3072
	v_add_co_u32_e32 v162, vcc, s93, v156
	v_cvt_pk_f32_fp8_sdwa v[192:193], v161 src0_sel:WORD_1
	s_nop 0
	v_addc_co_u32_e32 v163, vcc, 0, v157, vcc
	v_add_co_u32_e32 v156, vcc, s3, v156
	flat_load_dwordx2 v[186:187], v[162:163] offset:1024
	flat_load_dwordx2 v[184:185], v[162:163] offset:3072
	v_addc_co_u32_e32 v157, vcc, 0, v157, vcc
	flat_load_dwordx2 v[182:183], v[156:157] offset:1024
	flat_load_dwordx2 v[180:181], v[156:157] offset:3072
	v_cvt_pk_f32_fp8_e32 v[156:157], v160
	v_cvt_pk_f32_fp8_sdwa v[162:163], v160 src0_sel:WORD_1
	v_cvt_pk_f32_fp8_e32 v[160:161], v158
	v_cvt_pk_f32_fp8_sdwa v[198:199], v158 src0_sel:WORD_1
	v_fmamk_f32 v5, v156, 0x3d800000, v14
	v_mul_f32_e32 v5, 0xbfb8aa3b, v5
	v_exp_f32_e32 v5, v5
	v_cvt_pk_f32_fp8_e32 v[218:219], v159
	v_cvt_pk_f32_fp8_sdwa v[194:195], v159 src0_sel:WORD_1
	v_fmamk_f32 v156, v160, 0x3d800000, v18
	v_add_f32_e32 v5, 1.0, v5
	v_rcp_f32_e32 v158, v5
	v_fmamk_f32 v5, v157, 0x3d800000, v15
	v_mul_f32_e32 v5, 0xbfb8aa3b, v5
	v_exp_f32_e32 v5, v5
	v_fmamk_f32 v157, v161, 0x3d800000, v19
	v_mul_f32_e32 v156, 0xbfb8aa3b, v156
	v_mul_f32_e32 v157, 0xbfb8aa3b, v157
	v_add_f32_e32 v5, 1.0, v5
	v_rcp_f32_e32 v159, v5
	v_fmamk_f32 v5, v162, 0x3d800000, v16
	v_mul_f32_e32 v5, 0xbfb8aa3b, v5
	v_exp_f32_e32 v5, v5
	v_fmamk_f32 v160, v198, 0x3d800000, v20
	v_fmamk_f32 v161, v199, 0x3d800000, v21
	v_exp_f32_e32 v156, v156
	v_add_f32_e32 v5, 1.0, v5
	v_rcp_f32_e32 v162, v5
	v_fmamk_f32 v5, v163, 0x3d800000, v17
	v_mul_f32_e32 v5, 0xbfb8aa3b, v5
	v_exp_f32_e32 v5, v5
	v_exp_f32_e32 v157, v157
	v_mul_f32_e32 v160, 0xbfb8aa3b, v160
	v_mul_f32_e32 v161, 0xbfb8aa3b, v161
	v_add_f32_e32 v5, 1.0, v5
	v_rcp_f32_e32 v163, v5
	v_fmamk_f32 v5, v196, 0x3d800000, v6
	v_mul_f32_e32 v5, 0xbfb8aa3b, v5
	v_exp_f32_e32 v5, v5
	v_exp_f32_e32 v160, v160
	v_exp_f32_e32 v161, v161
	v_pk_add_f32 v[156:157], v[156:157], 1.0 op_sel_hi:[1,0]
	v_add_f32_e32 v5, 1.0, v5
	v_rcp_f32_e32 v196, v5
	v_fmamk_f32 v5, v197, 0x3d800000, v7
	v_mul_f32_e32 v5, 0xbfb8aa3b, v5
	v_exp_f32_e32 v5, v5
	v_pk_add_f32 v[160:161], v[160:161], 1.0 op_sel_hi:[1,0]
	v_pk_mul_f32 v[156:157], v[156:157], s[78:79] op_sel_hi:[1,0]
	v_pk_mul_f32 v[160:161], v[160:161], s[78:79] op_sel_hi:[1,0]
	v_add_f32_e32 v5, 1.0, v5
	v_rcp_f32_e32 v197, v5
	v_fmamk_f32 v5, v192, 0x3d800000, v8
	v_mul_f32_e32 v5, 0xbfb8aa3b, v5
	v_exp_f32_e32 v5, v5
	v_pk_mul_f32 v[156:157], v[158:159], v[156:157]
	v_pk_mul_f32 v[158:159], v[162:163], v[160:161]
	v_pk_mul_f32 v[146:147], v[146:147], v[156:157]
	v_fmamk_f32 v156, v218, 0x3d800000, v10
	v_add_f32_e32 v5, 1.0, v5
	v_pk_mul_f32 v[148:149], v[148:149], v[158:159]
	v_mul_f32_e32 v156, 0xbfb8aa3b, v156
	v_rcp_f32_e32 v158, v5
	v_fmamk_f32 v5, v193, 0x3d800000, v9
	v_exp_f32_e32 v198, v156
	v_fmamk_f32 v156, v219, 0x3d800000, v11
	v_mul_f32_e32 v5, 0xbfb8aa3b, v5
	v_mul_f32_e32 v156, 0xbfb8aa3b, v156
	v_exp_f32_e32 v5, v5
	v_exp_f32_e32 v199, v156
	v_fmamk_f32 v156, v194, 0x3d800000, v12
	v_fmamk_f32 v157, v195, 0x3d800000, v13
	v_mul_f32_e32 v156, 0xbfb8aa3b, v156
	v_mul_f32_e32 v157, 0xbfb8aa3b, v157
	v_exp_f32_e32 v156, v156
	v_exp_f32_e32 v157, v157
	v_add_f32_e32 v5, 1.0, v5
	v_rcp_f32_e32 v159, v5
	v_pk_add_f32 v[160:161], v[198:199], 1.0 op_sel_hi:[1,0]
	v_pk_add_f32 v[156:157], v[156:157], 1.0 op_sel_hi:[1,0]
	v_pk_mul_f32 v[160:161], v[160:161], s[78:79] op_sel_hi:[1,0]
	v_pk_mul_f32 v[156:157], v[156:157], s[78:79] op_sel_hi:[1,0]
	v_pk_mul_f32 v[160:161], v[196:197], v[160:161]
	v_pk_mul_f32 v[156:157], v[158:159], v[156:157]
	v_pk_mul_f32 v[142:143], v[142:143], v[160:161]
	v_pk_mul_f32 v[144:145], v[144:145], v[156:157]
	s_waitcnt vmcnt(0) lgkmcnt(0)
	v_cvt_pk_f32_fp8_e32 v[156:157], v190
	v_cvt_pk_f32_fp8_sdwa v[158:159], v190 src0_sel:WORD_1
	v_cvt_pk_f32_fp8_e32 v[160:161], v191
	v_cvt_pk_f32_fp8_sdwa v[162:163], v191 src0_sel:WORD_1
	v_fmamk_f32 v5, v156, 0x3d800000, v14
	v_mul_f32_e32 v5, 0xbfb8aa3b, v5
	v_exp_f32_e32 v5, v5
	v_cvt_pk_f32_fp8_e32 v[190:191], v188
	v_cvt_pk_f32_fp8_sdwa v[192:193], v188 src0_sel:WORD_1
	v_cvt_pk_f32_fp8_e32 v[194:195], v189
	v_add_f32_e32 v5, 1.0, v5
	v_fmamk_f32 v156, v190, 0x3d800000, v18
	v_rcp_f32_e32 v190, v5
	v_fmamk_f32 v5, v157, 0x3d800000, v15
	v_mul_f32_e32 v5, 0xbfb8aa3b, v5
	v_exp_f32_e32 v5, v5
	v_fmamk_f32 v157, v191, 0x3d800000, v19
	v_mul_f32_e32 v156, 0xbfb8aa3b, v156
	v_mul_f32_e32 v157, 0xbfb8aa3b, v157
	v_add_f32_e32 v5, 1.0, v5
	v_rcp_f32_e32 v191, v5
	v_fmamk_f32 v5, v158, 0x3d800000, v16
	v_mul_f32_e32 v5, 0xbfb8aa3b, v5
	v_exp_f32_e32 v5, v5
	v_fmamk_f32 v158, v192, 0x3d800000, v20
	v_mul_f32_e32 v158, 0xbfb8aa3b, v158
	v_exp_f32_e32 v158, v158
	v_add_f32_e32 v5, 1.0, v5
	v_rcp_f32_e32 v192, v5
	v_fmamk_f32 v5, v159, 0x3d800000, v17
	v_mul_f32_e32 v5, 0xbfb8aa3b, v5
	v_exp_f32_e32 v5, v5
	v_fmamk_f32 v159, v193, 0x3d800000, v21
	v_mul_f32_e32 v159, 0xbfb8aa3b, v159
	v_exp_f32_e32 v159, v159
	v_add_f32_e32 v5, 1.0, v5
	v_rcp_f32_e32 v193, v5
	v_fmamk_f32 v5, v160, 0x3d800000, v6
	v_mul_f32_e32 v5, 0xbfb8aa3b, v5
	v_exp_f32_e32 v5, v5
	v_pk_add_f32 v[158:159], v[158:159], 1.0 op_sel_hi:[1,0]
	v_exp_f32_e32 v156, v156
	v_pk_mul_f32 v[158:159], v[158:159], s[78:79] op_sel_hi:[1,0]
	v_add_f32_e32 v5, 1.0, v5
	v_pk_mul_f32 v[158:159], v[192:193], v[158:159]
	v_exp_f32_e32 v157, v157
	v_pk_mul_f32 v[140:141], v[140:141], v[158:159]
	v_rcp_f32_e32 v158, v5
	v_fmamk_f32 v5, v161, 0x3d800000, v7
	v_mul_f32_e32 v5, 0xbfb8aa3b, v5
	v_exp_f32_e32 v5, v5
	v_pk_add_f32 v[156:157], v[156:157], 1.0 op_sel_hi:[1,0]
	v_cvt_pk_f32_fp8_sdwa v[188:189], v189 src0_sel:WORD_1
	v_pk_mul_f32 v[156:157], v[156:157], s[78:79] op_sel_hi:[1,0]
	v_add_f32_e32 v5, 1.0, v5
	v_rcp_f32_e32 v159, v5
	v_fmamk_f32 v5, v162, 0x3d800000, v8
	v_mul_f32_e32 v5, 0xbfb8aa3b, v5
	v_pk_mul_f32 v[156:157], v[190:191], v[156:157]
	v_exp_f32_e32 v5, v5
	v_pk_mul_f32 v[138:139], v[138:139], v[156:157]
	v_fmamk_f32 v156, v194, 0x3d800000, v10
	v_fmamk_f32 v157, v195, 0x3d800000, v11
	v_mul_f32_e32 v156, 0xbfb8aa3b, v156
	v_mul_f32_e32 v157, 0xbfb8aa3b, v157
	v_exp_f32_e32 v156, v156
	v_exp_f32_e32 v157, v157
	v_add_f32_e32 v5, 1.0, v5
	v_rcp_f32_e32 v162, v5
	v_fmamk_f32 v5, v163, 0x3d800000, v9
	v_mul_f32_e32 v5, 0xbfb8aa3b, v5
	v_exp_f32_e32 v5, v5
	v_pk_add_f32 v[156:157], v[156:157], 1.0 op_sel_hi:[1,0]
	v_fmamk_f32 v160, v188, 0x3d800000, v12
	v_fmamk_f32 v161, v189, 0x3d800000, v13
	v_pk_mul_f32 v[156:157], v[156:157], s[78:79] op_sel_hi:[1,0]
	v_mul_f32_e32 v160, 0xbfb8aa3b, v160
	v_mul_f32_e32 v161, 0xbfb8aa3b, v161
	v_pk_mul_f32 v[156:157], v[158:159], v[156:157]
	v_exp_f32_e32 v160, v160
	v_exp_f32_e32 v161, v161
	v_pk_mul_f32 v[134:135], v[134:135], v[156:157]
	v_cvt_pk_f32_fp8_e32 v[156:157], v186
	v_add_f32_e32 v5, 1.0, v5
	v_rcp_f32_e32 v163, v5
	v_pk_add_f32 v[160:161], v[160:161], 1.0 op_sel_hi:[1,0]
	v_fmamk_f32 v5, v156, 0x3d800000, v14
	v_pk_mul_f32 v[160:161], v[160:161], s[78:79] op_sel_hi:[1,0]
	v_mul_f32_e32 v5, 0xbfb8aa3b, v5
	v_pk_mul_f32 v[158:159], v[162:163], v[160:161]
	v_exp_f32_e32 v5, v5
	v_pk_mul_f32 v[136:137], v[136:137], v[158:159]
	v_cvt_pk_f32_fp8_sdwa v[158:159], v186 src0_sel:WORD_1
	v_cvt_pk_f32_fp8_e32 v[160:161], v187
	v_cvt_pk_f32_fp8_sdwa v[162:163], v187 src0_sel:WORD_1
	v_cvt_pk_f32_fp8_e32 v[186:187], v184
	v_add_f32_e32 v5, 1.0, v5
	v_cvt_pk_f32_fp8_sdwa v[188:189], v184 src0_sel:WORD_1
	v_cvt_pk_f32_fp8_e32 v[190:191], v185
	v_fmamk_f32 v156, v186, 0x3d800000, v18
	v_rcp_f32_e32 v186, v5
	v_fmamk_f32 v5, v157, 0x3d800000, v15
	v_mul_f32_e32 v5, 0xbfb8aa3b, v5
	v_exp_f32_e32 v5, v5
	v_fmamk_f32 v157, v187, 0x3d800000, v19
	v_mul_f32_e32 v156, 0xbfb8aa3b, v156
	v_mul_f32_e32 v157, 0xbfb8aa3b, v157
	v_add_f32_e32 v5, 1.0, v5
	v_rcp_f32_e32 v187, v5
	v_fmamk_f32 v5, v158, 0x3d800000, v16
	v_mul_f32_e32 v5, 0xbfb8aa3b, v5
	v_exp_f32_e32 v5, v5
	v_fmamk_f32 v158, v188, 0x3d800000, v20
	v_mul_f32_e32 v158, 0xbfb8aa3b, v158
	v_exp_f32_e32 v158, v158
	v_add_f32_e32 v5, 1.0, v5
	v_rcp_f32_e32 v188, v5
	v_fmamk_f32 v5, v159, 0x3d800000, v17
	v_mul_f32_e32 v5, 0xbfb8aa3b, v5
	v_exp_f32_e32 v5, v5
	v_fmamk_f32 v159, v189, 0x3d800000, v21
	v_mul_f32_e32 v159, 0xbfb8aa3b, v159
	v_exp_f32_e32 v159, v159
	v_add_f32_e32 v5, 1.0, v5
	v_rcp_f32_e32 v189, v5
	v_fmamk_f32 v5, v160, 0x3d800000, v6
	v_mul_f32_e32 v5, 0xbfb8aa3b, v5
	v_exp_f32_e32 v5, v5
	v_pk_add_f32 v[158:159], v[158:159], 1.0 op_sel_hi:[1,0]
	v_exp_f32_e32 v156, v156
	v_pk_mul_f32 v[158:159], v[158:159], s[78:79] op_sel_hi:[1,0]
	v_add_f32_e32 v5, 1.0, v5
	v_pk_mul_f32 v[158:159], v[188:189], v[158:159]
	v_exp_f32_e32 v157, v157
	v_pk_mul_f32 v[132:133], v[132:133], v[158:159]
	v_rcp_f32_e32 v158, v5
	v_fmamk_f32 v5, v161, 0x3d800000, v7
	v_mul_f32_e32 v5, 0xbfb8aa3b, v5
	v_exp_f32_e32 v5, v5
	v_pk_add_f32 v[156:157], v[156:157], 1.0 op_sel_hi:[1,0]
	v_cvt_pk_f32_fp8_sdwa v[184:185], v185 src0_sel:WORD_1
	v_pk_mul_f32 v[156:157], v[156:157], s[78:79] op_sel_hi:[1,0]
	v_add_f32_e32 v5, 1.0, v5
	v_rcp_f32_e32 v159, v5
	v_fmamk_f32 v5, v162, 0x3d800000, v8
	v_mul_f32_e32 v5, 0xbfb8aa3b, v5
	v_pk_mul_f32 v[156:157], v[186:187], v[156:157]
	v_exp_f32_e32 v5, v5
	v_pk_mul_f32 v[130:131], v[130:131], v[156:157]
	v_fmamk_f32 v156, v190, 0x3d800000, v10
	v_fmamk_f32 v157, v191, 0x3d800000, v11
	v_mul_f32_e32 v156, 0xbfb8aa3b, v156
	v_mul_f32_e32 v157, 0xbfb8aa3b, v157
	v_exp_f32_e32 v156, v156
	v_exp_f32_e32 v157, v157
	v_add_f32_e32 v5, 1.0, v5
	v_rcp_f32_e32 v162, v5
	v_fmamk_f32 v5, v163, 0x3d800000, v9
	v_mul_f32_e32 v5, 0xbfb8aa3b, v5
	v_exp_f32_e32 v5, v5
	v_pk_add_f32 v[156:157], v[156:157], 1.0 op_sel_hi:[1,0]
	v_fmamk_f32 v160, v184, 0x3d800000, v12
	v_fmamk_f32 v161, v185, 0x3d800000, v13
	v_pk_mul_f32 v[156:157], v[156:157], s[78:79] op_sel_hi:[1,0]
	v_mul_f32_e32 v160, 0xbfb8aa3b, v160
	v_mul_f32_e32 v161, 0xbfb8aa3b, v161
	v_pk_mul_f32 v[156:157], v[158:159], v[156:157]
	v_exp_f32_e32 v160, v160
	v_exp_f32_e32 v161, v161
	v_pk_mul_f32 v[126:127], v[126:127], v[156:157]
	v_cvt_pk_f32_fp8_e32 v[156:157], v182
	v_add_f32_e32 v5, 1.0, v5
	v_rcp_f32_e32 v163, v5
	v_pk_add_f32 v[160:161], v[160:161], 1.0 op_sel_hi:[1,0]
	v_fmamk_f32 v5, v156, 0x3d800000, v14
	v_pk_mul_f32 v[160:161], v[160:161], s[78:79] op_sel_hi:[1,0]
	v_mul_f32_e32 v5, 0xbfb8aa3b, v5
	v_pk_mul_f32 v[158:159], v[162:163], v[160:161]
	v_exp_f32_e32 v5, v5
	v_pk_mul_f32 v[128:129], v[128:129], v[158:159]
	v_cvt_pk_f32_fp8_sdwa v[158:159], v182 src0_sel:WORD_1
	v_cvt_pk_f32_fp8_e32 v[160:161], v183
	v_cvt_pk_f32_fp8_sdwa v[162:163], v183 src0_sel:WORD_1
	v_cvt_pk_f32_fp8_e32 v[182:183], v180
	v_add_f32_e32 v5, 1.0, v5
	v_cvt_pk_f32_fp8_sdwa v[184:185], v180 src0_sel:WORD_1
	v_cvt_pk_f32_fp8_e32 v[186:187], v181
	v_fmamk_f32 v156, v182, 0x3d800000, v18
	v_rcp_f32_e32 v182, v5
	v_fmamk_f32 v5, v157, 0x3d800000, v15
	v_mul_f32_e32 v5, 0xbfb8aa3b, v5
	v_exp_f32_e32 v5, v5
	v_fmamk_f32 v157, v183, 0x3d800000, v19
	v_mul_f32_e32 v156, 0xbfb8aa3b, v156
	v_mul_f32_e32 v157, 0xbfb8aa3b, v157
	v_add_f32_e32 v5, 1.0, v5
	v_rcp_f32_e32 v183, v5
	v_fmamk_f32 v5, v158, 0x3d800000, v16
	v_mul_f32_e32 v5, 0xbfb8aa3b, v5
	v_exp_f32_e32 v5, v5
	v_fmamk_f32 v158, v184, 0x3d800000, v20
	v_mul_f32_e32 v158, 0xbfb8aa3b, v158
	v_exp_f32_e32 v158, v158
	v_add_f32_e32 v5, 1.0, v5
	v_rcp_f32_e32 v184, v5
	v_fmamk_f32 v5, v159, 0x3d800000, v17
	v_mul_f32_e32 v5, 0xbfb8aa3b, v5
	v_exp_f32_e32 v5, v5
	v_fmamk_f32 v159, v185, 0x3d800000, v21
	v_mul_f32_e32 v159, 0xbfb8aa3b, v159
	v_exp_f32_e32 v159, v159
	v_add_f32_e32 v5, 1.0, v5
	v_rcp_f32_e32 v185, v5
	v_fmamk_f32 v5, v160, 0x3d800000, v6
	v_mul_f32_e32 v5, 0xbfb8aa3b, v5
	v_exp_f32_e32 v5, v5
	v_exp_f32_e32 v156, v156
	v_exp_f32_e32 v157, v157
	v_pk_add_f32 v[158:159], v[158:159], 1.0 op_sel_hi:[1,0]
	v_add_f32_e32 v5, 1.0, v5
	v_pk_mul_f32 v[158:159], v[158:159], s[78:79] op_sel_hi:[1,0]
	v_pk_add_f32 v[156:157], v[156:157], 1.0 op_sel_hi:[1,0]
	v_pk_mul_f32 v[158:159], v[184:185], v[158:159]
	v_pk_mul_f32 v[156:157], v[156:157], s[78:79] op_sel_hi:[1,0]
	v_pk_mul_f32 v[124:125], v[124:125], v[158:159]
	v_rcp_f32_e32 v158, v5
	v_fmamk_f32 v5, v161, 0x3d800000, v7
	v_mul_f32_e32 v5, 0xbfb8aa3b, v5
	v_pk_mul_f32 v[156:157], v[182:183], v[156:157]
	v_exp_f32_e32 v5, v5
	v_pk_mul_f32 v[122:123], v[122:123], v[156:157]
	v_fmamk_f32 v156, v186, 0x3d800000, v10
	v_fmamk_f32 v157, v187, 0x3d800000, v11
	v_mul_f32_e32 v156, 0xbfb8aa3b, v156
	v_mul_f32_e32 v157, 0xbfb8aa3b, v157
	v_exp_f32_e32 v156, v156
	v_exp_f32_e32 v157, v157
	v_add_f32_e32 v5, 1.0, v5
	v_cvt_pk_f32_fp8_sdwa v[180:181], v181 src0_sel:WORD_1
	v_rcp_f32_e32 v159, v5
	v_pk_add_f32 v[156:157], v[156:157], 1.0 op_sel_hi:[1,0]
	v_fmamk_f32 v5, v162, 0x3d800000, v8
	v_pk_mul_f32 v[156:157], v[156:157], s[78:79] op_sel_hi:[1,0]
	v_fmamk_f32 v160, v180, 0x3d800000, v12
	v_fmamk_f32 v161, v181, 0x3d800000, v13
	v_pk_mul_f32 v[156:157], v[158:159], v[156:157]
	v_lshl_add_u64 v[180:181], v[178:179], 0, s[50:51]
	v_pk_mul_f32 v[118:119], v[118:119], v[156:157]
	v_mul_f32_e32 v5, 0xbfb8aa3b, v5
	v_add_co_u32_e32 v156, vcc, s31, v180
	v_exp_f32_e32 v5, v5
	s_nop 0
	v_addc_co_u32_e32 v157, vcc, 0, v181, vcc
	flat_load_dwordx2 v[192:193], v[156:157] offset:1024
	flat_load_dwordx2 v[194:195], v[156:157] offset:3072
	v_add_co_u32_e32 v156, vcc, s20, v180
	v_add_f32_e32 v5, 1.0, v5
	s_nop 0
	v_addc_co_u32_e32 v157, vcc, 0, v181, vcc
	flat_load_dwordx2 v[190:191], v[156:157] offset:1024
	flat_load_dwordx2 v[188:189], v[156:157] offset:3072
	v_rcp_f32_e32 v162, v5
	v_fmamk_f32 v5, v163, 0x3d800000, v9
	v_mul_f32_e32 v5, 0xbfb8aa3b, v5
	v_add_co_u32_e32 v156, vcc, s93, v180
	v_exp_f32_e32 v5, v5
	s_nop 0
	v_addc_co_u32_e32 v157, vcc, 0, v181, vcc
	flat_load_dwordx2 v[186:187], v[156:157] offset:1024
	flat_load_dwordx2 v[184:185], v[156:157] offset:3072
	v_add_co_u32_e32 v156, vcc, s3, v180
	v_mul_f32_e32 v160, 0xbfb8aa3b, v160
	v_mul_f32_e32 v161, 0xbfb8aa3b, v161
	v_addc_co_u32_e32 v157, vcc, 0, v181, vcc
	v_exp_f32_e32 v160, v160
	v_exp_f32_e32 v161, v161
	flat_load_dwordx2 v[182:183], v[156:157] offset:1024
	flat_load_dwordx2 v[180:181], v[156:157] offset:3072
	v_add_f32_e32 v5, 1.0, v5
	v_rcp_f32_e32 v163, v5
	v_pk_add_f32 v[160:161], v[160:161], 1.0 op_sel_hi:[1,0]
	s_mov_b64 s[50:51], 0x1a0080
	v_pk_mul_f32 v[160:161], v[160:161], s[78:79] op_sel_hi:[1,0]
	s_waitcnt vmcnt(0) lgkmcnt(0)
	v_cvt_pk_f32_fp8_e32 v[156:157], v192
	v_pk_mul_f32 v[158:159], v[162:163], v[160:161]
	v_cvt_pk_f32_fp8_e32 v[160:161], v193
	v_pk_mul_f32 v[120:121], v[120:121], v[158:159]
	v_fmamk_f32 v5, v156, 0x3d800000, v14
	v_mul_f32_e32 v5, 0xbfb8aa3b, v5
	v_exp_f32_e32 v5, v5
	v_cvt_pk_f32_fp8_sdwa v[158:159], v192 src0_sel:WORD_1
	v_cvt_pk_f32_fp8_sdwa v[162:163], v193 src0_sel:WORD_1
	v_cvt_pk_f32_fp8_e32 v[192:193], v194
	v_add_f32_e32 v5, 1.0, v5
	v_cvt_pk_f32_fp8_sdwa v[196:197], v194 src0_sel:WORD_1
	v_cvt_pk_f32_fp8_e32 v[198:199], v195
	v_fmamk_f32 v156, v192, 0x3d800000, v18
	v_rcp_f32_e32 v192, v5
	v_fmamk_f32 v5, v157, 0x3d800000, v15
	v_mul_f32_e32 v5, 0xbfb8aa3b, v5
	v_exp_f32_e32 v5, v5
	v_fmamk_f32 v157, v193, 0x3d800000, v19
	v_mul_f32_e32 v156, 0xbfb8aa3b, v156
	v_mul_f32_e32 v157, 0xbfb8aa3b, v157
	v_add_f32_e32 v5, 1.0, v5
	v_rcp_f32_e32 v193, v5
	v_fmamk_f32 v5, v158, 0x3d800000, v16
	v_mul_f32_e32 v5, 0xbfb8aa3b, v5
	v_exp_f32_e32 v5, v5
	v_fmamk_f32 v158, v196, 0x3d800000, v20
	v_mul_f32_e32 v158, 0xbfb8aa3b, v158
	v_exp_f32_e32 v158, v158
	v_add_f32_e32 v5, 1.0, v5
	v_rcp_f32_e32 v196, v5
	v_fmamk_f32 v5, v159, 0x3d800000, v17
	v_mul_f32_e32 v5, 0xbfb8aa3b, v5
	v_exp_f32_e32 v5, v5
	v_fmamk_f32 v159, v197, 0x3d800000, v21
	v_mul_f32_e32 v159, 0xbfb8aa3b, v159
	v_exp_f32_e32 v159, v159
	v_add_f32_e32 v5, 1.0, v5
	v_rcp_f32_e32 v197, v5
	v_fmamk_f32 v5, v160, 0x3d800000, v6
	v_mul_f32_e32 v5, 0xbfb8aa3b, v5
	v_exp_f32_e32 v5, v5
	v_pk_add_f32 v[158:159], v[158:159], 1.0 op_sel_hi:[1,0]
	v_exp_f32_e32 v156, v156
	v_pk_mul_f32 v[158:159], v[158:159], s[78:79] op_sel_hi:[1,0]
	v_add_f32_e32 v5, 1.0, v5
	v_pk_mul_f32 v[158:159], v[196:197], v[158:159]
	v_exp_f32_e32 v157, v157
	v_pk_mul_f32 v[116:117], v[116:117], v[158:159]
	v_rcp_f32_e32 v158, v5
	v_fmamk_f32 v5, v161, 0x3d800000, v7
	v_mul_f32_e32 v5, 0xbfb8aa3b, v5
	v_exp_f32_e32 v5, v5
	v_pk_add_f32 v[156:157], v[156:157], 1.0 op_sel_hi:[1,0]
	v_cvt_pk_f32_fp8_sdwa v[194:195], v195 src0_sel:WORD_1
	v_pk_mul_f32 v[156:157], v[156:157], s[78:79] op_sel_hi:[1,0]
	v_add_f32_e32 v5, 1.0, v5
	v_rcp_f32_e32 v159, v5
	v_fmamk_f32 v5, v162, 0x3d800000, v8
	v_mul_f32_e32 v5, 0xbfb8aa3b, v5
	v_pk_mul_f32 v[156:157], v[192:193], v[156:157]
	v_exp_f32_e32 v5, v5
	v_pk_mul_f32 v[114:115], v[114:115], v[156:157]
	v_fmamk_f32 v156, v198, 0x3d800000, v10
	v_fmamk_f32 v157, v199, 0x3d800000, v11
	v_mul_f32_e32 v156, 0xbfb8aa3b, v156
	v_mul_f32_e32 v157, 0xbfb8aa3b, v157
	v_exp_f32_e32 v156, v156
	v_exp_f32_e32 v157, v157
	v_add_f32_e32 v5, 1.0, v5
	v_rcp_f32_e32 v162, v5
	v_fmamk_f32 v5, v163, 0x3d800000, v9
	v_mul_f32_e32 v5, 0xbfb8aa3b, v5
	v_exp_f32_e32 v5, v5
	v_pk_add_f32 v[156:157], v[156:157], 1.0 op_sel_hi:[1,0]
	v_fmamk_f32 v160, v194, 0x3d800000, v12
	v_fmamk_f32 v161, v195, 0x3d800000, v13
	v_pk_mul_f32 v[156:157], v[156:157], s[78:79] op_sel_hi:[1,0]
	v_mul_f32_e32 v160, 0xbfb8aa3b, v160
	v_mul_f32_e32 v161, 0xbfb8aa3b, v161
	v_pk_mul_f32 v[156:157], v[158:159], v[156:157]
	v_exp_f32_e32 v160, v160
	v_exp_f32_e32 v161, v161
	v_pk_mul_f32 v[110:111], v[110:111], v[156:157]
	v_cvt_pk_f32_fp8_e32 v[156:157], v190
	v_add_f32_e32 v5, 1.0, v5
	v_rcp_f32_e32 v163, v5
	v_pk_add_f32 v[160:161], v[160:161], 1.0 op_sel_hi:[1,0]
	v_fmamk_f32 v5, v156, 0x3d800000, v14
	v_pk_mul_f32 v[160:161], v[160:161], s[78:79] op_sel_hi:[1,0]
	v_mul_f32_e32 v5, 0xbfb8aa3b, v5
	v_pk_mul_f32 v[158:159], v[162:163], v[160:161]
	v_exp_f32_e32 v5, v5
	v_pk_mul_f32 v[112:113], v[112:113], v[158:159]
	v_cvt_pk_f32_fp8_sdwa v[158:159], v190 src0_sel:WORD_1
	v_cvt_pk_f32_fp8_e32 v[160:161], v191
	v_cvt_pk_f32_fp8_sdwa v[162:163], v191 src0_sel:WORD_1
	v_cvt_pk_f32_fp8_e32 v[190:191], v188
	v_add_f32_e32 v5, 1.0, v5
	v_cvt_pk_f32_fp8_sdwa v[192:193], v188 src0_sel:WORD_1
	v_cvt_pk_f32_fp8_e32 v[194:195], v189
	v_fmamk_f32 v156, v190, 0x3d800000, v18
	v_rcp_f32_e32 v190, v5
	v_fmamk_f32 v5, v157, 0x3d800000, v15
	v_mul_f32_e32 v5, 0xbfb8aa3b, v5
	v_exp_f32_e32 v5, v5
	v_fmamk_f32 v157, v191, 0x3d800000, v19
	v_mul_f32_e32 v156, 0xbfb8aa3b, v156
	v_mul_f32_e32 v157, 0xbfb8aa3b, v157
	v_add_f32_e32 v5, 1.0, v5
	v_rcp_f32_e32 v191, v5
	v_fmamk_f32 v5, v158, 0x3d800000, v16
	v_mul_f32_e32 v5, 0xbfb8aa3b, v5
	v_exp_f32_e32 v5, v5
	v_fmamk_f32 v158, v192, 0x3d800000, v20
	v_mul_f32_e32 v158, 0xbfb8aa3b, v158
	v_exp_f32_e32 v158, v158
	v_add_f32_e32 v5, 1.0, v5
	v_rcp_f32_e32 v192, v5
	v_fmamk_f32 v5, v159, 0x3d800000, v17
	v_mul_f32_e32 v5, 0xbfb8aa3b, v5
	v_exp_f32_e32 v5, v5
	v_fmamk_f32 v159, v193, 0x3d800000, v21
	v_mul_f32_e32 v159, 0xbfb8aa3b, v159
	v_exp_f32_e32 v159, v159
	v_add_f32_e32 v5, 1.0, v5
	v_rcp_f32_e32 v193, v5
	v_fmamk_f32 v5, v160, 0x3d800000, v6
	v_mul_f32_e32 v5, 0xbfb8aa3b, v5
	v_exp_f32_e32 v5, v5
	v_pk_add_f32 v[158:159], v[158:159], 1.0 op_sel_hi:[1,0]
	v_exp_f32_e32 v156, v156
	v_pk_mul_f32 v[158:159], v[158:159], s[78:79] op_sel_hi:[1,0]
	v_add_f32_e32 v5, 1.0, v5
	v_pk_mul_f32 v[158:159], v[192:193], v[158:159]
	v_exp_f32_e32 v157, v157
	v_pk_mul_f32 v[108:109], v[108:109], v[158:159]
	v_rcp_f32_e32 v158, v5
	v_fmamk_f32 v5, v161, 0x3d800000, v7
	v_mul_f32_e32 v5, 0xbfb8aa3b, v5
	v_exp_f32_e32 v5, v5
	v_pk_add_f32 v[156:157], v[156:157], 1.0 op_sel_hi:[1,0]
	v_cvt_pk_f32_fp8_sdwa v[188:189], v189 src0_sel:WORD_1
	v_pk_mul_f32 v[156:157], v[156:157], s[78:79] op_sel_hi:[1,0]
	v_add_f32_e32 v5, 1.0, v5
	v_rcp_f32_e32 v159, v5
	v_fmamk_f32 v5, v162, 0x3d800000, v8
	v_mul_f32_e32 v5, 0xbfb8aa3b, v5
	v_pk_mul_f32 v[156:157], v[190:191], v[156:157]
	v_exp_f32_e32 v5, v5
	v_pk_mul_f32 v[106:107], v[106:107], v[156:157]
	v_fmamk_f32 v156, v194, 0x3d800000, v10
	v_fmamk_f32 v157, v195, 0x3d800000, v11
	v_mul_f32_e32 v156, 0xbfb8aa3b, v156
	v_mul_f32_e32 v157, 0xbfb8aa3b, v157
	v_exp_f32_e32 v156, v156
	v_exp_f32_e32 v157, v157
	v_add_f32_e32 v5, 1.0, v5
	v_rcp_f32_e32 v162, v5
	v_fmamk_f32 v5, v163, 0x3d800000, v9
	v_mul_f32_e32 v5, 0xbfb8aa3b, v5
	v_exp_f32_e32 v5, v5
	v_pk_add_f32 v[156:157], v[156:157], 1.0 op_sel_hi:[1,0]
	v_fmamk_f32 v160, v188, 0x3d800000, v12
	v_fmamk_f32 v161, v189, 0x3d800000, v13
	v_pk_mul_f32 v[156:157], v[156:157], s[78:79] op_sel_hi:[1,0]
	v_mul_f32_e32 v160, 0xbfb8aa3b, v160
	v_mul_f32_e32 v161, 0xbfb8aa3b, v161
	v_pk_mul_f32 v[156:157], v[158:159], v[156:157]
	v_exp_f32_e32 v160, v160
	v_exp_f32_e32 v161, v161
	v_pk_mul_f32 v[102:103], v[102:103], v[156:157]
	v_cvt_pk_f32_fp8_e32 v[156:157], v186
	v_add_f32_e32 v5, 1.0, v5
	v_rcp_f32_e32 v163, v5
	v_pk_add_f32 v[160:161], v[160:161], 1.0 op_sel_hi:[1,0]
	v_fmamk_f32 v5, v156, 0x3d800000, v14
	v_pk_mul_f32 v[160:161], v[160:161], s[78:79] op_sel_hi:[1,0]
	v_mul_f32_e32 v5, 0xbfb8aa3b, v5
	v_pk_mul_f32 v[158:159], v[162:163], v[160:161]
	v_exp_f32_e32 v5, v5
	v_pk_mul_f32 v[104:105], v[104:105], v[158:159]
	v_cvt_pk_f32_fp8_sdwa v[158:159], v186 src0_sel:WORD_1
	v_cvt_pk_f32_fp8_e32 v[160:161], v187
	v_cvt_pk_f32_fp8_sdwa v[162:163], v187 src0_sel:WORD_1
	v_cvt_pk_f32_fp8_e32 v[186:187], v184
	v_add_f32_e32 v5, 1.0, v5
	v_cvt_pk_f32_fp8_sdwa v[188:189], v184 src0_sel:WORD_1
	v_cvt_pk_f32_fp8_e32 v[190:191], v185
	v_fmamk_f32 v156, v186, 0x3d800000, v18
	v_rcp_f32_e32 v186, v5
	v_fmamk_f32 v5, v157, 0x3d800000, v15
	v_mul_f32_e32 v5, 0xbfb8aa3b, v5
	v_exp_f32_e32 v5, v5
	v_fmamk_f32 v157, v187, 0x3d800000, v19
	v_mul_f32_e32 v156, 0xbfb8aa3b, v156
	v_mul_f32_e32 v157, 0xbfb8aa3b, v157
	v_add_f32_e32 v5, 1.0, v5
	v_rcp_f32_e32 v187, v5
	v_fmamk_f32 v5, v158, 0x3d800000, v16
	v_mul_f32_e32 v5, 0xbfb8aa3b, v5
	v_exp_f32_e32 v5, v5
	v_fmamk_f32 v158, v188, 0x3d800000, v20
	v_mul_f32_e32 v158, 0xbfb8aa3b, v158
	v_exp_f32_e32 v158, v158
	v_add_f32_e32 v5, 1.0, v5
	v_rcp_f32_e32 v188, v5
	v_fmamk_f32 v5, v159, 0x3d800000, v17
	v_mul_f32_e32 v5, 0xbfb8aa3b, v5
	v_exp_f32_e32 v5, v5
	v_fmamk_f32 v159, v189, 0x3d800000, v21
	v_mul_f32_e32 v159, 0xbfb8aa3b, v159
	v_exp_f32_e32 v159, v159
	v_add_f32_e32 v5, 1.0, v5
	v_rcp_f32_e32 v189, v5
	v_fmamk_f32 v5, v160, 0x3d800000, v6
	v_mul_f32_e32 v5, 0xbfb8aa3b, v5
	v_exp_f32_e32 v5, v5
	v_pk_add_f32 v[158:159], v[158:159], 1.0 op_sel_hi:[1,0]
	v_exp_f32_e32 v156, v156
	v_pk_mul_f32 v[158:159], v[158:159], s[78:79] op_sel_hi:[1,0]
	v_add_f32_e32 v5, 1.0, v5
	v_pk_mul_f32 v[158:159], v[188:189], v[158:159]
	v_exp_f32_e32 v157, v157
	v_pk_mul_f32 v[100:101], v[100:101], v[158:159]
	v_rcp_f32_e32 v158, v5
	v_fmamk_f32 v5, v161, 0x3d800000, v7
	v_mul_f32_e32 v5, 0xbfb8aa3b, v5
	v_exp_f32_e32 v5, v5
	v_pk_add_f32 v[156:157], v[156:157], 1.0 op_sel_hi:[1,0]
	v_cvt_pk_f32_fp8_sdwa v[184:185], v185 src0_sel:WORD_1
	v_pk_mul_f32 v[156:157], v[156:157], s[78:79] op_sel_hi:[1,0]
	v_add_f32_e32 v5, 1.0, v5
	v_rcp_f32_e32 v159, v5
	v_fmamk_f32 v5, v162, 0x3d800000, v8
	v_mul_f32_e32 v5, 0xbfb8aa3b, v5
	v_pk_mul_f32 v[156:157], v[186:187], v[156:157]
	v_exp_f32_e32 v5, v5
	v_pk_mul_f32 v[98:99], v[98:99], v[156:157]
	v_fmamk_f32 v156, v190, 0x3d800000, v10
	v_fmamk_f32 v157, v191, 0x3d800000, v11
	v_mul_f32_e32 v156, 0xbfb8aa3b, v156
	v_mul_f32_e32 v157, 0xbfb8aa3b, v157
	v_exp_f32_e32 v156, v156
	v_exp_f32_e32 v157, v157
	v_add_f32_e32 v5, 1.0, v5
	v_rcp_f32_e32 v162, v5
	v_fmamk_f32 v5, v163, 0x3d800000, v9
	v_mul_f32_e32 v5, 0xbfb8aa3b, v5
	v_exp_f32_e32 v5, v5
	v_pk_add_f32 v[156:157], v[156:157], 1.0 op_sel_hi:[1,0]
	v_fmamk_f32 v160, v184, 0x3d800000, v12
	v_fmamk_f32 v161, v185, 0x3d800000, v13
	v_pk_mul_f32 v[156:157], v[156:157], s[78:79] op_sel_hi:[1,0]
	v_mul_f32_e32 v160, 0xbfb8aa3b, v160
	v_mul_f32_e32 v161, 0xbfb8aa3b, v161
	v_pk_mul_f32 v[156:157], v[158:159], v[156:157]
	v_exp_f32_e32 v160, v160
	v_exp_f32_e32 v161, v161
	v_pk_mul_f32 v[94:95], v[94:95], v[156:157]
	v_cvt_pk_f32_fp8_e32 v[156:157], v182
	v_add_f32_e32 v5, 1.0, v5
	v_rcp_f32_e32 v163, v5
	v_pk_add_f32 v[160:161], v[160:161], 1.0 op_sel_hi:[1,0]
	v_fmamk_f32 v5, v156, 0x3d800000, v14
	v_pk_mul_f32 v[160:161], v[160:161], s[78:79] op_sel_hi:[1,0]
	v_mul_f32_e32 v5, 0xbfb8aa3b, v5
	v_pk_mul_f32 v[158:159], v[162:163], v[160:161]
	v_exp_f32_e32 v5, v5
	v_pk_mul_f32 v[96:97], v[96:97], v[158:159]
	v_cvt_pk_f32_fp8_sdwa v[158:159], v182 src0_sel:WORD_1
	v_cvt_pk_f32_fp8_e32 v[160:161], v183
	v_cvt_pk_f32_fp8_sdwa v[162:163], v183 src0_sel:WORD_1
	v_cvt_pk_f32_fp8_e32 v[182:183], v180
	v_add_f32_e32 v5, 1.0, v5
	v_cvt_pk_f32_fp8_sdwa v[184:185], v180 src0_sel:WORD_1
	v_fmac_f32_e32 v17, 0x3d800000, v159
	v_fmamk_f32 v14, v182, 0x3d800000, v18
	v_rcp_f32_e32 v18, v5
	v_fmamk_f32 v5, v157, 0x3d800000, v15
	v_mul_f32_e32 v5, 0xbfb8aa3b, v5
	v_exp_f32_e32 v5, v5
	v_fmamk_f32 v15, v183, 0x3d800000, v19
	v_fmac_f32_e32 v21, 0x3d800000, v185
	v_cvt_pk_f32_fp8_e32 v[186:187], v181
	v_add_f32_e32 v5, 1.0, v5
	v_rcp_f32_e32 v19, v5
	v_fmamk_f32 v5, v158, 0x3d800000, v16
	v_mul_f32_e32 v5, 0xbfb8aa3b, v5
	v_exp_f32_e32 v5, v5
	v_fmamk_f32 v16, v184, 0x3d800000, v20
	v_mul_f32_e32 v16, 0xbfb8aa3b, v16
	v_exp_f32_e32 v20, v16
	v_add_f32_e32 v5, 1.0, v5
	v_rcp_f32_e32 v16, v5
	v_mul_f32_e32 v5, 0xbfb8aa3b, v21
	v_exp_f32_e32 v21, v5
	v_mul_f32_e32 v5, 0xbfb8aa3b, v17
	v_exp_f32_e32 v5, v5
	v_cvt_pk_f32_fp8_sdwa v[180:181], v181 src0_sel:WORD_1
	v_fmac_f32_e32 v9, 0x3d800000, v163
	v_mul_f32_e32 v14, 0xbfb8aa3b, v14
	v_add_f32_e32 v5, 1.0, v5
	v_rcp_f32_e32 v17, v5
	v_fmamk_f32 v5, v160, 0x3d800000, v6
	v_mul_f32_e32 v5, 0xbfb8aa3b, v5
	v_exp_f32_e32 v5, v5
	v_fmamk_f32 v6, v186, 0x3d800000, v10
	v_fmac_f32_e32 v13, 0x3d800000, v181
	v_mul_f32_e32 v15, 0xbfb8aa3b, v15
	v_add_f32_e32 v5, 1.0, v5
	v_rcp_f32_e32 v10, v5
	v_fmamk_f32 v5, v161, 0x3d800000, v7
	v_mul_f32_e32 v5, 0xbfb8aa3b, v5
	v_exp_f32_e32 v5, v5
	v_fmamk_f32 v7, v187, 0x3d800000, v11
	v_mul_f32_e32 v6, 0xbfb8aa3b, v6
	v_mul_f32_e32 v7, 0xbfb8aa3b, v7
	v_add_f32_e32 v5, 1.0, v5
	v_rcp_f32_e32 v11, v5
	v_fmamk_f32 v5, v162, 0x3d800000, v8
	v_mul_f32_e32 v5, 0xbfb8aa3b, v5
	v_exp_f32_e32 v5, v5
	v_fmamk_f32 v8, v180, 0x3d800000, v12
	v_mul_f32_e32 v8, 0xbfb8aa3b, v8
	v_exp_f32_e32 v12, v8
	v_add_f32_e32 v5, 1.0, v5
	v_rcp_f32_e32 v8, v5
	v_mul_f32_e32 v5, 0xbfb8aa3b, v13
	v_exp_f32_e32 v13, v5
	v_mul_f32_e32 v5, 0xbfb8aa3b, v9
	v_exp_f32_e32 v5, v5
	v_exp_f32_e32 v14, v14
	v_exp_f32_e32 v15, v15
	v_exp_f32_e32 v6, v6
	v_exp_f32_e32 v7, v7
	v_add_f32_e32 v5, 1.0, v5
	v_rcp_f32_e32 v9, v5
	v_pk_add_f32 v[14:15], v[14:15], 1.0 op_sel_hi:[1,0]
	v_pk_add_f32 v[20:21], v[20:21], 1.0 op_sel_hi:[1,0]
	v_pk_add_f32 v[6:7], v[6:7], 1.0 op_sel_hi:[1,0]
	v_pk_add_f32 v[12:13], v[12:13], 1.0 op_sel_hi:[1,0]
	v_pk_mul_f32 v[20:21], v[20:21], s[78:79] op_sel_hi:[1,0]
	v_pk_mul_f32 v[14:15], v[14:15], s[78:79] op_sel_hi:[1,0]
	v_pk_mul_f32 v[12:13], v[12:13], s[78:79] op_sel_hi:[1,0]
	v_pk_mul_f32 v[6:7], v[6:7], s[78:79] op_sel_hi:[1,0]
	v_pk_mul_f32 v[14:15], v[18:19], v[14:15]
	v_pk_mul_f32 v[16:17], v[16:17], v[20:21]
	v_pk_mul_f32 v[6:7], v[10:11], v[6:7]
	v_pk_mul_f32 v[8:9], v[8:9], v[12:13]
	v_lshl_add_u64 v[180:181], v[178:179], 0, s[86:87]
	v_pk_mul_f32 v[92:93], v[92:93], v[16:17]
	v_pk_mul_f32 v[90:91], v[90:91], v[14:15]
	v_pk_mul_f32 v[88:89], v[88:89], v[8:9]
	v_pk_mul_f32 v[86:87], v[86:87], v[6:7]
	global_load_dwordx4 v[6:9], v[168:169], off offset:528
	global_load_dwordx4 v[14:17], v[168:169], off offset:512
	global_load_dwordx4 v[10:13], v[170:171], off offset:16
	global_load_dwordx4 v[18:21], v[170:171], off
	v_lshl_add_u64 v[178:179], v[178:179], 0, s[50:51]
	v_add_co_u32_e32 v156, vcc, s31, v180
	s_nop 1
	v_addc_co_u32_e32 v157, vcc, 0, v181, vcc
	flat_load_dwordx2 v[192:193], v[156:157] offset:1024
	flat_load_dwordx2 v[194:195], v[156:157] offset:3072
	v_add_co_u32_e32 v156, vcc, s20, v180
	s_waitcnt vmcnt(0) lgkmcnt(0)
	v_cvt_pk_f32_fp8_sdwa v[158:159], v192 src0_sel:WORD_1
	v_addc_co_u32_e32 v157, vcc, 0, v181, vcc
	flat_load_dwordx2 v[190:191], v[156:157] offset:1024
	flat_load_dwordx2 v[188:189], v[156:157] offset:3072
	v_add_co_u32_e32 v156, vcc, s93, v180
	v_cvt_pk_f32_fp8_e32 v[160:161], v193
	s_nop 0
	v_addc_co_u32_e32 v157, vcc, 0, v181, vcc
	flat_load_dwordx2 v[186:187], v[156:157] offset:1024
	flat_load_dwordx2 v[184:185], v[156:157] offset:3072
	v_add_co_u32_e32 v156, vcc, s3, v180
	v_cvt_pk_f32_fp8_sdwa v[162:163], v193 src0_sel:WORD_1
	s_nop 0
	v_addc_co_u32_e32 v157, vcc, 0, v181, vcc
	flat_load_dwordx2 v[182:183], v[156:157] offset:1024
	flat_load_dwordx2 v[180:181], v[156:157] offset:3072
	v_cvt_pk_f32_fp8_e32 v[156:157], v192
	v_cvt_pk_f32_fp8_e32 v[192:193], v194
	v_cvt_pk_f32_fp8_sdwa v[196:197], v194 src0_sel:WORD_1
	v_cvt_pk_f32_fp8_e32 v[198:199], v195
	v_fmamk_f32 v5, v156, 0x3d800000, v14
	v_mul_f32_e32 v5, 0xbfb8aa3b, v5
	v_exp_f32_e32 v5, v5
	v_fmamk_f32 v156, v192, 0x3d800000, v18
	v_mul_f32_e32 v156, 0xbfb8aa3b, v156
	v_exp_f32_e32 v156, v156
	v_add_f32_e32 v5, 1.0, v5
	v_rcp_f32_e32 v192, v5
	v_fmamk_f32 v5, v157, 0x3d800000, v15
	v_mul_f32_e32 v5, 0xbfb8aa3b, v5
	v_exp_f32_e32 v5, v5
	v_fmamk_f32 v157, v193, 0x3d800000, v19
	v_mul_f32_e32 v157, 0xbfb8aa3b, v157
	v_exp_f32_e32 v157, v157
	v_add_f32_e32 v5, 1.0, v5
	v_rcp_f32_e32 v193, v5
	v_fmamk_f32 v5, v158, 0x3d800000, v16
	v_mul_f32_e32 v5, 0xbfb8aa3b, v5
	v_exp_f32_e32 v5, v5
	v_fmamk_f32 v158, v196, 0x3d800000, v20
	v_mul_f32_e32 v158, 0xbfb8aa3b, v158
	v_exp_f32_e32 v158, v158
	v_add_f32_e32 v5, 1.0, v5
	v_rcp_f32_e32 v196, v5
	v_fmamk_f32 v5, v159, 0x3d800000, v17
	v_mul_f32_e32 v5, 0xbfb8aa3b, v5
	v_exp_f32_e32 v5, v5
	v_fmamk_f32 v159, v197, 0x3d800000, v21
	v_mul_f32_e32 v159, 0xbfb8aa3b, v159
	v_exp_f32_e32 v159, v159
	v_add_f32_e32 v5, 1.0, v5
	v_rcp_f32_e32 v197, v5
	v_fmamk_f32 v5, v160, 0x3d800000, v6
	v_mul_f32_e32 v5, 0xbfb8aa3b, v5
	v_exp_f32_e32 v5, v5
	v_pk_add_f32 v[158:159], v[158:159], 1.0 op_sel_hi:[1,0]
	v_pk_add_f32 v[156:157], v[156:157], 1.0 op_sel_hi:[1,0]
	v_pk_mul_f32 v[158:159], v[158:159], s[78:79] op_sel_hi:[1,0]
	v_add_f32_e32 v5, 1.0, v5
	v_pk_mul_f32 v[158:159], v[196:197], v[158:159]
	v_pk_mul_f32 v[156:157], v[156:157], s[78:79] op_sel_hi:[1,0]
	v_pk_mul_f32 v[84:85], v[84:85], v[158:159]
	v_rcp_f32_e32 v158, v5
	v_fmamk_f32 v5, v161, 0x3d800000, v7
	v_mul_f32_e32 v5, 0xbfb8aa3b, v5
	v_exp_f32_e32 v5, v5
	v_pk_mul_f32 v[156:157], v[192:193], v[156:157]
	v_cvt_pk_f32_fp8_sdwa v[194:195], v195 src0_sel:WORD_1
	v_pk_mul_f32 v[82:83], v[82:83], v[156:157]
	v_add_f32_e32 v5, 1.0, v5
	v_rcp_f32_e32 v159, v5
	v_fmamk_f32 v5, v162, 0x3d800000, v8
	v_mul_f32_e32 v5, 0xbfb8aa3b, v5
	v_exp_f32_e32 v5, v5
	v_fmamk_f32 v156, v198, 0x3d800000, v10
	v_fmamk_f32 v157, v199, 0x3d800000, v11
	v_mul_f32_e32 v156, 0xbfb8aa3b, v156
	v_mul_f32_e32 v157, 0xbfb8aa3b, v157
	v_exp_f32_e32 v156, v156
	v_exp_f32_e32 v157, v157
	v_add_f32_e32 v5, 1.0, v5
	v_rcp_f32_e32 v162, v5
	v_fmamk_f32 v5, v163, 0x3d800000, v9
	v_mul_f32_e32 v5, 0xbfb8aa3b, v5
	v_exp_f32_e32 v5, v5
	v_pk_add_f32 v[156:157], v[156:157], 1.0 op_sel_hi:[1,0]
	v_fmamk_f32 v160, v194, 0x3d800000, v12
	v_fmamk_f32 v161, v195, 0x3d800000, v13
	v_pk_mul_f32 v[156:157], v[156:157], s[78:79] op_sel_hi:[1,0]
	v_mul_f32_e32 v160, 0xbfb8aa3b, v160
	v_mul_f32_e32 v161, 0xbfb8aa3b, v161
	v_pk_mul_f32 v[156:157], v[158:159], v[156:157]
	v_exp_f32_e32 v160, v160
	v_exp_f32_e32 v161, v161
	v_pk_mul_f32 v[78:79], v[78:79], v[156:157]
	s_waitcnt vmcnt(0) lgkmcnt(0)
	v_cvt_pk_f32_fp8_e32 v[156:157], v190
	v_add_f32_e32 v5, 1.0, v5
	v_rcp_f32_e32 v163, v5
	v_pk_add_f32 v[160:161], v[160:161], 1.0 op_sel_hi:[1,0]
	v_fmamk_f32 v5, v156, 0x3d800000, v14
	v_pk_mul_f32 v[160:161], v[160:161], s[78:79] op_sel_hi:[1,0]
	v_mul_f32_e32 v5, 0xbfb8aa3b, v5
	v_pk_mul_f32 v[158:159], v[162:163], v[160:161]
	v_exp_f32_e32 v5, v5
	v_pk_mul_f32 v[80:81], v[80:81], v[158:159]
	v_cvt_pk_f32_fp8_sdwa v[158:159], v190 src0_sel:WORD_1
	v_cvt_pk_f32_fp8_e32 v[160:161], v191
	v_cvt_pk_f32_fp8_sdwa v[162:163], v191 src0_sel:WORD_1
	v_cvt_pk_f32_fp8_e32 v[190:191], v188
	v_add_f32_e32 v5, 1.0, v5
	v_cvt_pk_f32_fp8_sdwa v[192:193], v188 src0_sel:WORD_1
	v_cvt_pk_f32_fp8_e32 v[194:195], v189
	v_fmamk_f32 v156, v190, 0x3d800000, v18
	v_rcp_f32_e32 v190, v5
	v_fmamk_f32 v5, v157, 0x3d800000, v15
	v_mul_f32_e32 v5, 0xbfb8aa3b, v5
	v_exp_f32_e32 v5, v5
	v_fmamk_f32 v157, v191, 0x3d800000, v19
	v_mul_f32_e32 v156, 0xbfb8aa3b, v156
	v_mul_f32_e32 v157, 0xbfb8aa3b, v157
	v_add_f32_e32 v5, 1.0, v5
	v_rcp_f32_e32 v191, v5
	v_fmamk_f32 v5, v158, 0x3d800000, v16
	v_mul_f32_e32 v5, 0xbfb8aa3b, v5
	v_exp_f32_e32 v5, v5
	v_fmamk_f32 v158, v192, 0x3d800000, v20
	v_mul_f32_e32 v158, 0xbfb8aa3b, v158
	v_exp_f32_e32 v158, v158
	v_add_f32_e32 v5, 1.0, v5
	v_rcp_f32_e32 v192, v5
	v_fmamk_f32 v5, v159, 0x3d800000, v17
	v_mul_f32_e32 v5, 0xbfb8aa3b, v5
	v_exp_f32_e32 v5, v5
	v_fmamk_f32 v159, v193, 0x3d800000, v21
	v_mul_f32_e32 v159, 0xbfb8aa3b, v159
	v_exp_f32_e32 v159, v159
	v_add_f32_e32 v5, 1.0, v5
	v_rcp_f32_e32 v193, v5
	v_fmamk_f32 v5, v160, 0x3d800000, v6
	v_mul_f32_e32 v5, 0xbfb8aa3b, v5
	v_exp_f32_e32 v5, v5
	v_pk_add_f32 v[158:159], v[158:159], 1.0 op_sel_hi:[1,0]
	v_exp_f32_e32 v156, v156
	v_pk_mul_f32 v[158:159], v[158:159], s[78:79] op_sel_hi:[1,0]
	v_add_f32_e32 v5, 1.0, v5
	v_pk_mul_f32 v[158:159], v[192:193], v[158:159]
	v_exp_f32_e32 v157, v157
	v_pk_mul_f32 v[76:77], v[76:77], v[158:159]
	v_rcp_f32_e32 v158, v5
	v_fmamk_f32 v5, v161, 0x3d800000, v7
	v_mul_f32_e32 v5, 0xbfb8aa3b, v5
	v_exp_f32_e32 v5, v5
	v_pk_add_f32 v[156:157], v[156:157], 1.0 op_sel_hi:[1,0]
	v_cvt_pk_f32_fp8_sdwa v[188:189], v189 src0_sel:WORD_1
	v_pk_mul_f32 v[156:157], v[156:157], s[78:79] op_sel_hi:[1,0]
	v_add_f32_e32 v5, 1.0, v5
	v_rcp_f32_e32 v159, v5
	v_fmamk_f32 v5, v162, 0x3d800000, v8
	v_mul_f32_e32 v5, 0xbfb8aa3b, v5
	v_pk_mul_f32 v[156:157], v[190:191], v[156:157]
	v_exp_f32_e32 v5, v5
	v_pk_mul_f32 v[74:75], v[74:75], v[156:157]
	v_fmamk_f32 v156, v194, 0x3d800000, v10
	v_fmamk_f32 v157, v195, 0x3d800000, v11
	v_mul_f32_e32 v156, 0xbfb8aa3b, v156
	v_mul_f32_e32 v157, 0xbfb8aa3b, v157
	v_exp_f32_e32 v156, v156
	v_exp_f32_e32 v157, v157
	v_add_f32_e32 v5, 1.0, v5
	v_rcp_f32_e32 v162, v5
	v_fmamk_f32 v5, v163, 0x3d800000, v9
	v_mul_f32_e32 v5, 0xbfb8aa3b, v5
	v_exp_f32_e32 v5, v5
	v_pk_add_f32 v[156:157], v[156:157], 1.0 op_sel_hi:[1,0]
	v_fmamk_f32 v160, v188, 0x3d800000, v12
	v_fmamk_f32 v161, v189, 0x3d800000, v13
	v_pk_mul_f32 v[156:157], v[156:157], s[78:79] op_sel_hi:[1,0]
	v_mul_f32_e32 v160, 0xbfb8aa3b, v160
	v_mul_f32_e32 v161, 0xbfb8aa3b, v161
	v_pk_mul_f32 v[156:157], v[158:159], v[156:157]
	v_exp_f32_e32 v160, v160
	v_exp_f32_e32 v161, v161
	v_pk_mul_f32 v[70:71], v[70:71], v[156:157]
	v_cvt_pk_f32_fp8_e32 v[156:157], v186
	v_add_f32_e32 v5, 1.0, v5
	v_rcp_f32_e32 v163, v5
	v_pk_add_f32 v[160:161], v[160:161], 1.0 op_sel_hi:[1,0]
	v_fmamk_f32 v5, v156, 0x3d800000, v14
	v_pk_mul_f32 v[160:161], v[160:161], s[78:79] op_sel_hi:[1,0]
	v_mul_f32_e32 v5, 0xbfb8aa3b, v5
	v_pk_mul_f32 v[158:159], v[162:163], v[160:161]
	v_exp_f32_e32 v5, v5
	v_pk_mul_f32 v[72:73], v[72:73], v[158:159]
	v_cvt_pk_f32_fp8_sdwa v[158:159], v186 src0_sel:WORD_1
	v_cvt_pk_f32_fp8_e32 v[160:161], v187
	v_cvt_pk_f32_fp8_sdwa v[162:163], v187 src0_sel:WORD_1
	v_cvt_pk_f32_fp8_e32 v[186:187], v184
	v_add_f32_e32 v5, 1.0, v5
	v_cvt_pk_f32_fp8_sdwa v[188:189], v184 src0_sel:WORD_1
	v_cvt_pk_f32_fp8_e32 v[190:191], v185
	v_fmamk_f32 v156, v186, 0x3d800000, v18
	v_rcp_f32_e32 v186, v5
	v_fmamk_f32 v5, v157, 0x3d800000, v15
	v_mul_f32_e32 v5, 0xbfb8aa3b, v5
	v_exp_f32_e32 v5, v5
	v_fmamk_f32 v157, v187, 0x3d800000, v19
	v_mul_f32_e32 v156, 0xbfb8aa3b, v156
	v_mul_f32_e32 v157, 0xbfb8aa3b, v157
	v_add_f32_e32 v5, 1.0, v5
	v_rcp_f32_e32 v187, v5
	v_fmamk_f32 v5, v158, 0x3d800000, v16
	v_mul_f32_e32 v5, 0xbfb8aa3b, v5
	v_exp_f32_e32 v5, v5
	v_fmamk_f32 v158, v188, 0x3d800000, v20
	v_mul_f32_e32 v158, 0xbfb8aa3b, v158
	v_exp_f32_e32 v158, v158
	v_add_f32_e32 v5, 1.0, v5
	v_rcp_f32_e32 v188, v5
	v_fmamk_f32 v5, v159, 0x3d800000, v17
	v_mul_f32_e32 v5, 0xbfb8aa3b, v5
	v_exp_f32_e32 v5, v5
	v_fmamk_f32 v159, v189, 0x3d800000, v21
	v_mul_f32_e32 v159, 0xbfb8aa3b, v159
	v_exp_f32_e32 v159, v159
	v_add_f32_e32 v5, 1.0, v5
	v_rcp_f32_e32 v189, v5
	v_fmamk_f32 v5, v160, 0x3d800000, v6
	v_mul_f32_e32 v5, 0xbfb8aa3b, v5
	v_exp_f32_e32 v5, v5
	v_pk_add_f32 v[158:159], v[158:159], 1.0 op_sel_hi:[1,0]
	v_exp_f32_e32 v156, v156
	v_pk_mul_f32 v[158:159], v[158:159], s[78:79] op_sel_hi:[1,0]
	v_add_f32_e32 v5, 1.0, v5
	v_pk_mul_f32 v[158:159], v[188:189], v[158:159]
	v_exp_f32_e32 v157, v157
	v_pk_mul_f32 v[68:69], v[68:69], v[158:159]
	v_rcp_f32_e32 v158, v5
	v_fmamk_f32 v5, v161, 0x3d800000, v7
	v_mul_f32_e32 v5, 0xbfb8aa3b, v5
	v_exp_f32_e32 v5, v5
	v_pk_add_f32 v[156:157], v[156:157], 1.0 op_sel_hi:[1,0]
	v_cvt_pk_f32_fp8_sdwa v[184:185], v185 src0_sel:WORD_1
	v_pk_mul_f32 v[156:157], v[156:157], s[78:79] op_sel_hi:[1,0]
	v_add_f32_e32 v5, 1.0, v5
	v_rcp_f32_e32 v159, v5
	v_fmamk_f32 v5, v162, 0x3d800000, v8
	v_mul_f32_e32 v5, 0xbfb8aa3b, v5
	v_pk_mul_f32 v[156:157], v[186:187], v[156:157]
	v_exp_f32_e32 v5, v5
	v_pk_mul_f32 v[66:67], v[66:67], v[156:157]
	v_fmamk_f32 v156, v190, 0x3d800000, v10
	v_fmamk_f32 v157, v191, 0x3d800000, v11
	v_mul_f32_e32 v156, 0xbfb8aa3b, v156
	v_mul_f32_e32 v157, 0xbfb8aa3b, v157
	v_exp_f32_e32 v156, v156
	v_exp_f32_e32 v157, v157
	v_add_f32_e32 v5, 1.0, v5
	v_rcp_f32_e32 v162, v5
	v_fmamk_f32 v5, v163, 0x3d800000, v9
	v_mul_f32_e32 v5, 0xbfb8aa3b, v5
	v_exp_f32_e32 v5, v5
	v_pk_add_f32 v[156:157], v[156:157], 1.0 op_sel_hi:[1,0]
	v_fmamk_f32 v160, v184, 0x3d800000, v12
	v_fmamk_f32 v161, v185, 0x3d800000, v13
	v_pk_mul_f32 v[156:157], v[156:157], s[78:79] op_sel_hi:[1,0]
	v_mul_f32_e32 v160, 0xbfb8aa3b, v160
	v_mul_f32_e32 v161, 0xbfb8aa3b, v161
	v_pk_mul_f32 v[156:157], v[158:159], v[156:157]
	v_exp_f32_e32 v160, v160
	v_exp_f32_e32 v161, v161
	v_pk_mul_f32 v[62:63], v[62:63], v[156:157]
	v_cvt_pk_f32_fp8_e32 v[156:157], v182
	v_add_f32_e32 v5, 1.0, v5
	v_rcp_f32_e32 v163, v5
	v_pk_add_f32 v[160:161], v[160:161], 1.0 op_sel_hi:[1,0]
	v_fmamk_f32 v5, v156, 0x3d800000, v14
	v_pk_mul_f32 v[160:161], v[160:161], s[78:79] op_sel_hi:[1,0]
	v_mul_f32_e32 v5, 0xbfb8aa3b, v5
	v_pk_mul_f32 v[158:159], v[162:163], v[160:161]
	v_exp_f32_e32 v5, v5
	v_pk_mul_f32 v[64:65], v[64:65], v[158:159]
	v_cvt_pk_f32_fp8_sdwa v[158:159], v182 src0_sel:WORD_1
	v_cvt_pk_f32_fp8_e32 v[160:161], v183
	v_cvt_pk_f32_fp8_sdwa v[162:163], v183 src0_sel:WORD_1
	v_cvt_pk_f32_fp8_e32 v[182:183], v180
	v_add_f32_e32 v5, 1.0, v5
	v_cvt_pk_f32_fp8_sdwa v[184:185], v180 src0_sel:WORD_1
	v_cvt_pk_f32_fp8_e32 v[186:187], v181
	v_fmamk_f32 v156, v182, 0x3d800000, v18
	v_rcp_f32_e32 v182, v5
	v_fmamk_f32 v5, v157, 0x3d800000, v15
	v_mul_f32_e32 v5, 0xbfb8aa3b, v5
	v_exp_f32_e32 v5, v5
	v_fmamk_f32 v157, v183, 0x3d800000, v19
	v_mul_f32_e32 v156, 0xbfb8aa3b, v156
	v_mul_f32_e32 v157, 0xbfb8aa3b, v157
	v_add_f32_e32 v5, 1.0, v5
	v_rcp_f32_e32 v183, v5
	v_fmamk_f32 v5, v158, 0x3d800000, v16
	v_mul_f32_e32 v5, 0xbfb8aa3b, v5
	v_exp_f32_e32 v5, v5
	v_fmamk_f32 v158, v184, 0x3d800000, v20
	v_mul_f32_e32 v158, 0xbfb8aa3b, v158
	v_exp_f32_e32 v158, v158
	v_add_f32_e32 v5, 1.0, v5
	v_rcp_f32_e32 v184, v5
	v_fmamk_f32 v5, v159, 0x3d800000, v17
	v_mul_f32_e32 v5, 0xbfb8aa3b, v5
	v_exp_f32_e32 v5, v5
	v_fmamk_f32 v159, v185, 0x3d800000, v21
	v_mul_f32_e32 v159, 0xbfb8aa3b, v159
	v_exp_f32_e32 v159, v159
	v_add_f32_e32 v5, 1.0, v5
	v_rcp_f32_e32 v185, v5
	v_fmamk_f32 v5, v160, 0x3d800000, v6
	v_mul_f32_e32 v5, 0xbfb8aa3b, v5
	v_exp_f32_e32 v5, v5
	v_exp_f32_e32 v156, v156
	v_exp_f32_e32 v157, v157
	v_pk_add_f32 v[158:159], v[158:159], 1.0 op_sel_hi:[1,0]
	v_add_f32_e32 v5, 1.0, v5
	v_pk_mul_f32 v[158:159], v[158:159], s[78:79] op_sel_hi:[1,0]
	v_pk_add_f32 v[156:157], v[156:157], 1.0 op_sel_hi:[1,0]
	v_pk_mul_f32 v[158:159], v[184:185], v[158:159]
	v_pk_mul_f32 v[156:157], v[156:157], s[78:79] op_sel_hi:[1,0]
	v_pk_mul_f32 v[60:61], v[60:61], v[158:159]
	v_rcp_f32_e32 v158, v5
	v_fmamk_f32 v5, v161, 0x3d800000, v7
	v_mul_f32_e32 v5, 0xbfb8aa3b, v5
	v_pk_mul_f32 v[156:157], v[182:183], v[156:157]
	v_exp_f32_e32 v5, v5
	v_pk_mul_f32 v[58:59], v[58:59], v[156:157]
	v_fmamk_f32 v156, v186, 0x3d800000, v10
	v_fmamk_f32 v157, v187, 0x3d800000, v11
	v_mul_f32_e32 v156, 0xbfb8aa3b, v156
	v_mul_f32_e32 v157, 0xbfb8aa3b, v157
	v_exp_f32_e32 v156, v156
	v_exp_f32_e32 v157, v157
	v_add_f32_e32 v5, 1.0, v5
	v_rcp_f32_e32 v159, v5
	v_pk_add_f32 v[156:157], v[156:157], 1.0 op_sel_hi:[1,0]
	v_fmamk_f32 v5, v162, 0x3d800000, v8
	v_pk_mul_f32 v[156:157], v[156:157], s[78:79] op_sel_hi:[1,0]
	v_mul_f32_e32 v5, 0xbfb8aa3b, v5
	v_pk_mul_f32 v[156:157], v[158:159], v[156:157]
	v_exp_f32_e32 v5, v5
	v_pk_mul_f32 v[54:55], v[54:55], v[156:157]
	v_add_co_u32_e32 v156, vcc, s31, v178
	v_cvt_pk_f32_fp8_sdwa v[180:181], v181 src0_sel:WORD_1
	s_nop 0
	v_addc_co_u32_e32 v157, vcc, 0, v179, vcc
	flat_load_dwordx2 v[190:191], v[156:157] offset:1024
	flat_load_dwordx2 v[192:193], v[156:157] offset:3072
	v_add_co_u32_e32 v156, vcc, s20, v178
	v_add_f32_e32 v5, 1.0, v5
	s_nop 0
	v_addc_co_u32_e32 v157, vcc, 0, v179, vcc
	flat_load_dwordx2 v[188:189], v[156:157] offset:1024
	flat_load_dwordx2 v[186:187], v[156:157] offset:3072
	v_rcp_f32_e32 v162, v5
	v_fmamk_f32 v5, v163, 0x3d800000, v9
	v_mul_f32_e32 v5, 0xbfb8aa3b, v5
	v_add_co_u32_e32 v156, vcc, s93, v178
	v_exp_f32_e32 v5, v5
	s_nop 0
	v_addc_co_u32_e32 v157, vcc, 0, v179, vcc
	v_fmamk_f32 v160, v180, 0x3d800000, v12
	v_fmamk_f32 v161, v181, 0x3d800000, v13
	flat_load_dwordx2 v[184:185], v[156:157] offset:1024
	flat_load_dwordx2 v[182:183], v[156:157] offset:3072
	v_add_co_u32_e32 v156, vcc, s3, v178
	v_mul_f32_e32 v160, 0xbfb8aa3b, v160
	v_mul_f32_e32 v161, 0xbfb8aa3b, v161
	v_addc_co_u32_e32 v157, vcc, 0, v179, vcc
	v_exp_f32_e32 v160, v160
	v_exp_f32_e32 v161, v161
	flat_load_dwordx2 v[180:181], v[156:157] offset:1024
	flat_load_dwordx2 v[178:179], v[156:157] offset:3072
	v_add_f32_e32 v5, 1.0, v5
	v_rcp_f32_e32 v163, v5
	v_pk_add_f32 v[160:161], v[160:161], 1.0 op_sel_hi:[1,0]
	s_waitcnt vmcnt(0) lgkmcnt(0)
	v_cvt_pk_f32_fp8_e32 v[156:157], v190
	v_pk_mul_f32 v[160:161], v[160:161], s[78:79] op_sel_hi:[1,0]
	v_cvt_pk_f32_fp8_sdwa v[194:195], v192 src0_sel:WORD_1
	v_pk_mul_f32 v[158:159], v[162:163], v[160:161]
	v_fmamk_f32 v5, v156, 0x3d800000, v14
	v_mul_f32_e32 v5, 0xbfb8aa3b, v5
	v_exp_f32_e32 v5, v5
	v_pk_mul_f32 v[56:57], v[56:57], v[158:159]
	v_cvt_pk_f32_fp8_sdwa v[158:159], v190 src0_sel:WORD_1
	v_cvt_pk_f32_fp8_e32 v[160:161], v191
	v_cvt_pk_f32_fp8_sdwa v[162:163], v191 src0_sel:WORD_1
	v_cvt_pk_f32_fp8_e32 v[190:191], v192
	v_add_f32_e32 v5, 1.0, v5
	v_cvt_pk_f32_fp8_e32 v[196:197], v193
	v_cvt_pk_f32_fp8_sdwa v[192:193], v193 src0_sel:WORD_1
	v_fmamk_f32 v156, v190, 0x3d800000, v18
	v_rcp_f32_e32 v190, v5
	v_fmamk_f32 v5, v157, 0x3d800000, v15
	v_mul_f32_e32 v5, 0xbfb8aa3b, v5
	v_exp_f32_e32 v5, v5
	v_fmamk_f32 v157, v191, 0x3d800000, v19
	v_mul_f32_e32 v156, 0xbfb8aa3b, v156
	v_mul_f32_e32 v157, 0xbfb8aa3b, v157
	v_add_f32_e32 v5, 1.0, v5
	v_rcp_f32_e32 v191, v5
	v_fmamk_f32 v5, v158, 0x3d800000, v16
	v_mul_f32_e32 v5, 0xbfb8aa3b, v5
	v_exp_f32_e32 v5, v5
	v_fmamk_f32 v158, v194, 0x3d800000, v20
	v_mul_f32_e32 v158, 0xbfb8aa3b, v158
	v_exp_f32_e32 v158, v158
	v_add_f32_e32 v5, 1.0, v5
	v_rcp_f32_e32 v194, v5
	v_fmamk_f32 v5, v159, 0x3d800000, v17
	v_mul_f32_e32 v5, 0xbfb8aa3b, v5
	v_exp_f32_e32 v5, v5
	v_fmamk_f32 v159, v195, 0x3d800000, v21
	v_mul_f32_e32 v159, 0xbfb8aa3b, v159
	v_exp_f32_e32 v159, v159
	v_add_f32_e32 v5, 1.0, v5
	v_rcp_f32_e32 v195, v5
	v_fmamk_f32 v5, v160, 0x3d800000, v6
	v_mul_f32_e32 v5, 0xbfb8aa3b, v5
	v_exp_f32_e32 v5, v5
	v_pk_add_f32 v[158:159], v[158:159], 1.0 op_sel_hi:[1,0]
	v_exp_f32_e32 v156, v156
	v_pk_mul_f32 v[158:159], v[158:159], s[78:79] op_sel_hi:[1,0]
	v_add_f32_e32 v5, 1.0, v5
	v_pk_mul_f32 v[158:159], v[194:195], v[158:159]
	v_exp_f32_e32 v157, v157
	v_pk_mul_f32 v[52:53], v[52:53], v[158:159]
	v_rcp_f32_e32 v158, v5
	v_fmamk_f32 v5, v161, 0x3d800000, v7
	v_mul_f32_e32 v5, 0xbfb8aa3b, v5
	v_exp_f32_e32 v5, v5
	v_pk_add_f32 v[156:157], v[156:157], 1.0 op_sel_hi:[1,0]
	v_fmamk_f32 v160, v192, 0x3d800000, v12
	v_pk_mul_f32 v[156:157], v[156:157], s[78:79] op_sel_hi:[1,0]
	v_add_f32_e32 v5, 1.0, v5
	v_rcp_f32_e32 v159, v5
	v_fmamk_f32 v5, v162, 0x3d800000, v8
	v_mul_f32_e32 v5, 0xbfb8aa3b, v5
	v_pk_mul_f32 v[156:157], v[190:191], v[156:157]
	v_exp_f32_e32 v5, v5
	v_pk_mul_f32 v[50:51], v[50:51], v[156:157]
	v_fmamk_f32 v156, v196, 0x3d800000, v10
	v_fmamk_f32 v157, v197, 0x3d800000, v11
	v_mul_f32_e32 v156, 0xbfb8aa3b, v156
	v_mul_f32_e32 v157, 0xbfb8aa3b, v157
	v_exp_f32_e32 v156, v156
	v_exp_f32_e32 v157, v157
	v_add_f32_e32 v5, 1.0, v5
	v_rcp_f32_e32 v162, v5
	v_fmamk_f32 v5, v163, 0x3d800000, v9
	v_mul_f32_e32 v5, 0xbfb8aa3b, v5
	v_exp_f32_e32 v5, v5
	v_pk_add_f32 v[156:157], v[156:157], 1.0 op_sel_hi:[1,0]
	v_fmamk_f32 v161, v193, 0x3d800000, v13
	v_pk_mul_f32 v[156:157], v[156:157], s[78:79] op_sel_hi:[1,0]
	v_mul_f32_e32 v160, 0xbfb8aa3b, v160
	v_mul_f32_e32 v161, 0xbfb8aa3b, v161
	v_pk_mul_f32 v[156:157], v[158:159], v[156:157]
	v_exp_f32_e32 v160, v160
	v_exp_f32_e32 v161, v161
	v_pk_mul_f32 v[46:47], v[46:47], v[156:157]
	v_cvt_pk_f32_fp8_e32 v[156:157], v188
	v_add_f32_e32 v5, 1.0, v5
	v_rcp_f32_e32 v163, v5
	v_pk_add_f32 v[160:161], v[160:161], 1.0 op_sel_hi:[1,0]
	v_fmamk_f32 v5, v156, 0x3d800000, v14
	v_pk_mul_f32 v[160:161], v[160:161], s[78:79] op_sel_hi:[1,0]
	v_mul_f32_e32 v5, 0xbfb8aa3b, v5
	v_pk_mul_f32 v[158:159], v[162:163], v[160:161]
	v_exp_f32_e32 v5, v5
	v_pk_mul_f32 v[48:49], v[48:49], v[158:159]
	v_cvt_pk_f32_fp8_sdwa v[158:159], v188 src0_sel:WORD_1
	v_cvt_pk_f32_fp8_e32 v[160:161], v189
	v_cvt_pk_f32_fp8_sdwa v[162:163], v189 src0_sel:WORD_1
	v_cvt_pk_f32_fp8_e32 v[188:189], v186
	v_add_f32_e32 v5, 1.0, v5
	v_cvt_pk_f32_fp8_sdwa v[190:191], v186 src0_sel:WORD_1
	v_cvt_pk_f32_fp8_e32 v[192:193], v187
	v_fmamk_f32 v156, v188, 0x3d800000, v18
	v_rcp_f32_e32 v188, v5
	v_fmamk_f32 v5, v157, 0x3d800000, v15
	v_mul_f32_e32 v5, 0xbfb8aa3b, v5
	v_exp_f32_e32 v5, v5
	v_fmamk_f32 v157, v189, 0x3d800000, v19
	v_mul_f32_e32 v156, 0xbfb8aa3b, v156
	v_mul_f32_e32 v157, 0xbfb8aa3b, v157
	v_add_f32_e32 v5, 1.0, v5
	v_rcp_f32_e32 v189, v5
	v_fmamk_f32 v5, v158, 0x3d800000, v16
	v_mul_f32_e32 v5, 0xbfb8aa3b, v5
	v_exp_f32_e32 v5, v5
	v_fmamk_f32 v158, v190, 0x3d800000, v20
	v_mul_f32_e32 v158, 0xbfb8aa3b, v158
	v_exp_f32_e32 v158, v158
	v_add_f32_e32 v5, 1.0, v5
	v_rcp_f32_e32 v190, v5
	v_fmamk_f32 v5, v159, 0x3d800000, v17
	v_mul_f32_e32 v5, 0xbfb8aa3b, v5
	v_exp_f32_e32 v5, v5
	v_fmamk_f32 v159, v191, 0x3d800000, v21
	v_mul_f32_e32 v159, 0xbfb8aa3b, v159
	v_exp_f32_e32 v159, v159
	v_add_f32_e32 v5, 1.0, v5
	v_rcp_f32_e32 v191, v5
	v_fmamk_f32 v5, v160, 0x3d800000, v6
	v_mul_f32_e32 v5, 0xbfb8aa3b, v5
	v_exp_f32_e32 v5, v5
	v_pk_add_f32 v[158:159], v[158:159], 1.0 op_sel_hi:[1,0]
	v_exp_f32_e32 v156, v156
	v_pk_mul_f32 v[158:159], v[158:159], s[78:79] op_sel_hi:[1,0]
	v_add_f32_e32 v5, 1.0, v5
	v_pk_mul_f32 v[158:159], v[190:191], v[158:159]
	v_exp_f32_e32 v157, v157
	v_pk_mul_f32 v[44:45], v[44:45], v[158:159]
	v_rcp_f32_e32 v158, v5
	v_fmamk_f32 v5, v161, 0x3d800000, v7
	v_mul_f32_e32 v5, 0xbfb8aa3b, v5
	v_exp_f32_e32 v5, v5
	v_pk_add_f32 v[156:157], v[156:157], 1.0 op_sel_hi:[1,0]
	v_cvt_pk_f32_fp8_sdwa v[186:187], v187 src0_sel:WORD_1
	v_pk_mul_f32 v[156:157], v[156:157], s[78:79] op_sel_hi:[1,0]
	v_add_f32_e32 v5, 1.0, v5
	v_rcp_f32_e32 v159, v5
	v_fmamk_f32 v5, v162, 0x3d800000, v8
	v_mul_f32_e32 v5, 0xbfb8aa3b, v5
	v_pk_mul_f32 v[156:157], v[188:189], v[156:157]
	v_exp_f32_e32 v5, v5
	v_pk_mul_f32 v[42:43], v[42:43], v[156:157]
	v_fmamk_f32 v156, v192, 0x3d800000, v10
	v_fmamk_f32 v157, v193, 0x3d800000, v11
	v_mul_f32_e32 v156, 0xbfb8aa3b, v156
	v_mul_f32_e32 v157, 0xbfb8aa3b, v157
	v_exp_f32_e32 v156, v156
	v_exp_f32_e32 v157, v157
	v_add_f32_e32 v5, 1.0, v5
	v_rcp_f32_e32 v162, v5
	v_fmamk_f32 v5, v163, 0x3d800000, v9
	v_mul_f32_e32 v5, 0xbfb8aa3b, v5
	v_exp_f32_e32 v5, v5
	v_pk_add_f32 v[156:157], v[156:157], 1.0 op_sel_hi:[1,0]
	v_fmamk_f32 v160, v186, 0x3d800000, v12
	v_fmamk_f32 v161, v187, 0x3d800000, v13
	v_pk_mul_f32 v[156:157], v[156:157], s[78:79] op_sel_hi:[1,0]
	v_mul_f32_e32 v160, 0xbfb8aa3b, v160
	v_mul_f32_e32 v161, 0xbfb8aa3b, v161
	v_pk_mul_f32 v[156:157], v[158:159], v[156:157]
	v_exp_f32_e32 v160, v160
	v_exp_f32_e32 v161, v161
	v_pk_mul_f32 v[38:39], v[38:39], v[156:157]
	v_cvt_pk_f32_fp8_e32 v[156:157], v184
	v_add_f32_e32 v5, 1.0, v5
	v_rcp_f32_e32 v163, v5
	v_pk_add_f32 v[160:161], v[160:161], 1.0 op_sel_hi:[1,0]
	v_fmamk_f32 v5, v156, 0x3d800000, v14
	v_pk_mul_f32 v[160:161], v[160:161], s[78:79] op_sel_hi:[1,0]
	v_mul_f32_e32 v5, 0xbfb8aa3b, v5
	v_pk_mul_f32 v[158:159], v[162:163], v[160:161]
	v_exp_f32_e32 v5, v5
	v_pk_mul_f32 v[40:41], v[40:41], v[158:159]
	v_cvt_pk_f32_fp8_sdwa v[158:159], v184 src0_sel:WORD_1
	v_cvt_pk_f32_fp8_e32 v[160:161], v185
	v_cvt_pk_f32_fp8_sdwa v[162:163], v185 src0_sel:WORD_1
	v_cvt_pk_f32_fp8_e32 v[184:185], v182
	v_add_f32_e32 v5, 1.0, v5
	v_cvt_pk_f32_fp8_sdwa v[186:187], v182 src0_sel:WORD_1
	v_cvt_pk_f32_fp8_e32 v[188:189], v183
	v_fmamk_f32 v156, v184, 0x3d800000, v18
	v_rcp_f32_e32 v184, v5
	v_fmamk_f32 v5, v157, 0x3d800000, v15
	v_mul_f32_e32 v5, 0xbfb8aa3b, v5
	v_exp_f32_e32 v5, v5
	v_fmamk_f32 v157, v185, 0x3d800000, v19
	v_mul_f32_e32 v156, 0xbfb8aa3b, v156
	v_mul_f32_e32 v157, 0xbfb8aa3b, v157
	v_add_f32_e32 v5, 1.0, v5
	v_rcp_f32_e32 v185, v5
	v_fmamk_f32 v5, v158, 0x3d800000, v16
	v_mul_f32_e32 v5, 0xbfb8aa3b, v5
	v_exp_f32_e32 v5, v5
	v_fmamk_f32 v158, v186, 0x3d800000, v20
	v_mul_f32_e32 v158, 0xbfb8aa3b, v158
	v_exp_f32_e32 v158, v158
	v_add_f32_e32 v5, 1.0, v5
	v_rcp_f32_e32 v186, v5
	v_fmamk_f32 v5, v159, 0x3d800000, v17
	v_mul_f32_e32 v5, 0xbfb8aa3b, v5
	v_exp_f32_e32 v5, v5
	v_fmamk_f32 v159, v187, 0x3d800000, v21
	v_mul_f32_e32 v159, 0xbfb8aa3b, v159
	v_exp_f32_e32 v159, v159
	v_add_f32_e32 v5, 1.0, v5
	v_rcp_f32_e32 v187, v5
	v_fmamk_f32 v5, v160, 0x3d800000, v6
	v_mul_f32_e32 v5, 0xbfb8aa3b, v5
	v_exp_f32_e32 v5, v5
	v_pk_add_f32 v[158:159], v[158:159], 1.0 op_sel_hi:[1,0]
	v_exp_f32_e32 v156, v156
	v_pk_mul_f32 v[158:159], v[158:159], s[78:79] op_sel_hi:[1,0]
	v_add_f32_e32 v5, 1.0, v5
	v_pk_mul_f32 v[158:159], v[186:187], v[158:159]
	v_exp_f32_e32 v157, v157
	v_pk_mul_f32 v[36:37], v[36:37], v[158:159]
	v_rcp_f32_e32 v158, v5
	v_fmamk_f32 v5, v161, 0x3d800000, v7
	v_mul_f32_e32 v5, 0xbfb8aa3b, v5
	v_exp_f32_e32 v5, v5
	v_pk_add_f32 v[156:157], v[156:157], 1.0 op_sel_hi:[1,0]
	v_cvt_pk_f32_fp8_sdwa v[182:183], v183 src0_sel:WORD_1
	v_pk_mul_f32 v[156:157], v[156:157], s[78:79] op_sel_hi:[1,0]
	v_add_f32_e32 v5, 1.0, v5
	v_rcp_f32_e32 v159, v5
	v_fmamk_f32 v5, v162, 0x3d800000, v8
	v_pk_mul_f32 v[156:157], v[184:185], v[156:157]
	v_mul_f32_e32 v5, 0xbfb8aa3b, v5
	v_pk_mul_f32 v[34:35], v[34:35], v[156:157]
	v_fmamk_f32 v156, v188, 0x3d800000, v10
	v_fmamk_f32 v157, v189, 0x3d800000, v11
	v_exp_f32_e32 v5, v5
	v_mul_f32_e32 v156, 0xbfb8aa3b, v156
	v_mul_f32_e32 v157, 0xbfb8aa3b, v157
	v_exp_f32_e32 v156, v156
	v_exp_f32_e32 v157, v157
	v_add_f32_e32 v5, 1.0, v5
	v_rcp_f32_e32 v162, v5
	v_fmamk_f32 v5, v163, 0x3d800000, v9
	v_mul_f32_e32 v5, 0xbfb8aa3b, v5
	v_pk_add_f32 v[156:157], v[156:157], 1.0 op_sel_hi:[1,0]
	v_exp_f32_e32 v5, v5
	v_pk_mul_f32 v[156:157], v[156:157], s[78:79] op_sel_hi:[1,0]
	v_fmamk_f32 v160, v182, 0x3d800000, v12
	v_fmamk_f32 v161, v183, 0x3d800000, v13
	v_pk_mul_f32 v[156:157], v[158:159], v[156:157]
	v_mul_f32_e32 v160, 0xbfb8aa3b, v160
	v_mul_f32_e32 v161, 0xbfb8aa3b, v161
	v_pk_mul_f32 v[30:31], v[30:31], v[156:157]
	v_cvt_pk_f32_fp8_e32 v[156:157], v180
	v_exp_f32_e32 v160, v160
	v_exp_f32_e32 v161, v161
	v_add_f32_e32 v5, 1.0, v5
	v_rcp_f32_e32 v163, v5
	v_fmamk_f32 v5, v156, 0x3d800000, v14
	v_pk_add_f32 v[160:161], v[160:161], 1.0 op_sel_hi:[1,0]
	v_mul_f32_e32 v5, 0xbfb8aa3b, v5
	v_pk_mul_f32 v[160:161], v[160:161], s[78:79] op_sel_hi:[1,0]
	v_exp_f32_e32 v5, v5
	v_pk_mul_f32 v[158:159], v[162:163], v[160:161]
	v_cvt_pk_f32_fp8_e32 v[162:163], v178
	v_pk_mul_f32 v[32:33], v[32:33], v[158:159]
	v_add_f32_e32 v5, 1.0, v5
	v_cvt_pk_f32_fp8_sdwa v[158:159], v180 src0_sel:WORD_1
	v_fmamk_f32 v14, v162, 0x3d800000, v18
	v_rcp_f32_e32 v18, v5
	v_fmamk_f32 v5, v157, 0x3d800000, v15
	v_mul_f32_e32 v5, 0xbfb8aa3b, v5
	v_exp_f32_e32 v5, v5
	v_fmamk_f32 v15, v163, 0x3d800000, v19
	v_cvt_pk_f32_fp8_sdwa v[182:183], v178 src0_sel:WORD_1
	v_fmac_f32_e32 v17, 0x3d800000, v159
	v_add_f32_e32 v5, 1.0, v5
	v_rcp_f32_e32 v19, v5
	v_fmamk_f32 v5, v158, 0x3d800000, v16
	v_mul_f32_e32 v5, 0xbfb8aa3b, v5
	v_exp_f32_e32 v5, v5
	v_fmamk_f32 v16, v182, 0x3d800000, v20
	v_mul_f32_e32 v16, 0xbfb8aa3b, v16
	v_fmac_f32_e32 v21, 0x3d800000, v183
	v_add_f32_e32 v5, 1.0, v5
	v_exp_f32_e32 v20, v16
	v_rcp_f32_e32 v16, v5
	v_mul_f32_e32 v5, 0xbfb8aa3b, v21
	v_exp_f32_e32 v21, v5
	v_mul_f32_e32 v5, 0xbfb8aa3b, v17
	v_exp_f32_e32 v5, v5
	v_cvt_pk_f32_fp8_e32 v[160:161], v181
	v_cvt_pk_f32_fp8_e32 v[184:185], v179
	v_cvt_pk_f32_fp8_sdwa v[180:181], v181 src0_sel:WORD_1
	v_add_f32_e32 v5, 1.0, v5
	v_rcp_f32_e32 v17, v5
	v_fmamk_f32 v5, v160, 0x3d800000, v6
	v_mul_f32_e32 v5, 0xbfb8aa3b, v5
	v_exp_f32_e32 v5, v5
	v_fmamk_f32 v6, v184, 0x3d800000, v10
	v_cvt_pk_f32_fp8_sdwa v[178:179], v179 src0_sel:WORD_1
	v_fmac_f32_e32 v9, 0x3d800000, v181
	v_add_f32_e32 v5, 1.0, v5
	v_rcp_f32_e32 v10, v5
	v_fmamk_f32 v5, v161, 0x3d800000, v7
	v_mul_f32_e32 v5, 0xbfb8aa3b, v5
	v_exp_f32_e32 v5, v5
	v_fmamk_f32 v7, v185, 0x3d800000, v11
	v_fmac_f32_e32 v13, 0x3d800000, v179
	v_mul_f32_e32 v14, 0xbfb8aa3b, v14
	v_add_f32_e32 v5, 1.0, v5
	v_rcp_f32_e32 v11, v5
	v_fmamk_f32 v5, v180, 0x3d800000, v8
	v_mul_f32_e32 v5, 0xbfb8aa3b, v5
	v_exp_f32_e32 v5, v5
	v_fmamk_f32 v8, v178, 0x3d800000, v12
	v_mul_f32_e32 v8, 0xbfb8aa3b, v8
	v_exp_f32_e32 v12, v8
	v_add_f32_e32 v5, 1.0, v5
	v_rcp_f32_e32 v8, v5
	v_mul_f32_e32 v5, 0xbfb8aa3b, v13
	v_exp_f32_e32 v13, v5
	v_mul_f32_e32 v5, 0xbfb8aa3b, v9
	v_exp_f32_e32 v5, v5
	v_mul_f32_e32 v15, 0xbfb8aa3b, v15
	v_mul_f32_e32 v6, 0xbfb8aa3b, v6
	v_mul_f32_e32 v7, 0xbfb8aa3b, v7
	v_exp_f32_e32 v14, v14
	v_exp_f32_e32 v15, v15
	v_exp_f32_e32 v6, v6
	v_exp_f32_e32 v7, v7
	v_add_f32_e32 v5, 1.0, v5
	v_rcp_f32_e32 v9, v5
	v_pk_add_f32 v[14:15], v[14:15], 1.0 op_sel_hi:[1,0]
	v_pk_add_f32 v[20:21], v[20:21], 1.0 op_sel_hi:[1,0]
	v_pk_add_f32 v[6:7], v[6:7], 1.0 op_sel_hi:[1,0]
	v_pk_add_f32 v[12:13], v[12:13], 1.0 op_sel_hi:[1,0]
	v_pk_mul_f32 v[20:21], v[20:21], s[78:79] op_sel_hi:[1,0]
	v_pk_mul_f32 v[14:15], v[14:15], s[78:79] op_sel_hi:[1,0]
	v_pk_mul_f32 v[12:13], v[12:13], s[78:79] op_sel_hi:[1,0]
	v_pk_mul_f32 v[6:7], v[6:7], s[78:79] op_sel_hi:[1,0]
	v_pk_mul_f32 v[14:15], v[18:19], v[14:15]
	v_pk_mul_f32 v[16:17], v[16:17], v[20:21]
	v_pk_mul_f32 v[6:7], v[10:11], v[6:7]
	v_pk_mul_f32 v[8:9], v[8:9], v[12:13]
	v_pk_mul_f32 v[28:29], v[28:29], v[16:17]
	v_pk_mul_f32 v[26:27], v[26:27], v[14:15]
	v_pk_mul_f32 v[24:25], v[24:25], v[8:9]
	v_pk_mul_f32 v[22:23], v[22:23], v[6:7]
